# MoE GEMMs: f32 expert-weight tiles loaded with dwordx4 (no nt) + v_permlane32_swap repack instead of dwordx2 nt loads; plus batched ssm carry loads
# speedup vs baseline: 1.0234x; 1.0153x over previous
.LBB0_997:
	s_or_b64 exec, exec, s[64:65]
	s_mov_b32 s0, s37
	s_waitcnt lgkmcnt(0)
	s_barrier
	s_mov_b32 s1, s33
	v_mbcnt_lo_u32_b32 v0, -1, s0
	v_mbcnt_hi_u32_b32 v0, -1, v0
	v_lshl_or_b32 v0, s1, 6, v0
	v_readlane_b32 s0, v254, 0
	s_mov_b32 s16, s0
	s_mov_b32 s0, s37
	s_add_i32 s0, s0, 0x20120
	v_mov_b32_e32 v1, s0
	s_mov_b32 s0, 0
	ds_read_b64 v[2:3], v1
	s_add_i32 s0, s0, 0x200e0
	v_mov_b32_e32 v1, s0
	s_mov_b32 s0, s60
	s_mov_b32 s5, 0
	ds_read_b64 v[4:5], v1
	s_add_i32 s5, s5, 0x200e8
	v_readlane_b32 s1, v254, 1
	v_mov_b32_e32 v1, s5
	s_mov_b32 s8, s60
	s_mov_b32 s5, 0
	s_waitcnt lgkmcnt(0)
	v_readfirstlane_b32 s1, v3
	v_readfirstlane_b32 s4, v2
	ds_read_b64 v[2:3], v1
	s_add_i32 s5, s5, 0x20120
	v_mov_b32_e32 v1, s5
	v_readlane_b32 s5, v255, 10
	v_readfirstlane_b32 s2, v5
	v_readfirstlane_b32 s6, v4
	ds_read_b64 v[4:5], v1
	v_mov_b32_e32 v1, s5
	ds_read_b32 v158, v1
	s_waitcnt lgkmcnt(0)
	v_readfirstlane_b32 s10, v3
	v_readfirstlane_b32 s14, v2
	v_readfirstlane_b32 s11, v5
	v_readfirstlane_b32 s13, v4
	v_readfirstlane_b32 s5, v158
	s_lshl_b32 s5, s5, 3
	s_add_i32 s17, s5, 56
	s_andn2_b32 s17, s17, 63
	s_cmp_ge_i32 s16, s17
	v_readfirstlane_b32 s12, v0
	s_cbranch_scc1 .LBB0_1004
	s_add_u32 s4, s4, 0x1e79fd00
	s_addc_u32 s5, s1, 0
	s_ashr_i32 s1, s0, 31
	s_lshl_b64 s[0:1], s[0:1], 28
	s_add_u32 s6, s6, s0
	s_addc_u32 s7, s2, s1
	s_ashr_i32 s9, s8, 31
	s_lshl_b64 s[0:1], s[8:9], 28
	s_add_u32 s8, s14, s0
	s_addc_u32 s9, s10, s1
	s_add_u32 s10, s13, 0x2779fd00
	s_addc_u32 s11, s11, 0
	s_ashr_i32 s2, s12, 6
	v_bfe_u32 v2, v0, 4, 2
	v_and_b32_e32 v3, 7, v0
	s_lshl_b32 s0, s2, 5
	v_bitop3_b32 v3, v2, v3, 4 bitop3:0x36
	v_bitop3_b32 v2, v2, v0, 7 bitop3:0x78
	s_and_b32 s14, s0, 32
	s_ashr_i32 s0, s12, 7
	v_and_b32_e32 v1, 63, v0
	v_lshlrev_b32_e32 v161, 4, v2
	v_and_b32_e32 v2, 15, v0
	s_mulk_i32 s0, 0x50
	v_lshlrev_b32_e32 v160, 4, v3
	v_or_b32_e32 v3, s14, v2
	v_or_b32_e32 v162, s0, v2
	v_lshlrev_b32_e32 v2, 1, v1
	v_or_b32_e32 v4, 1, v2
	v_bitop3_b32 v5, s2, v4, 7 bitop3:0x78
	v_lshlrev_b32_e32 v4, 7, v4
	v_ashrrev_i32_e32 v159, 3, v0
	v_lshl_add_u32 v163, v5, 4, v4
	v_bitop3_b32 v2, s2, v2, 6 bitop3:0x78
	v_lshlrev_b32_e32 v4, 8, v1
	v_lshl_add_u32 v164, v2, 4, v4
	v_xor_b32_e32 v2, v159, v0
	v_lshlrev_b32_e32 v2, 4, v2
	v_lshlrev_b32_e32 v4, 7, v159
	s_movk_i32 s0, 0x70
	v_and_or_b32 v5, v2, s0, v4
	v_lshlrev_b32_e32 v2, 3, v0
	v_cmp_lt_u32_e64 s[0:1], 31, v1
	v_lshlrev_b32_e32 v1, 1, v0
	s_lshl_b32 s12, s2, 3
	v_and_b32_e32 v6, 16, v0
	v_lshrrev_b32_e32 v0, 2, v0
	v_lshlrev_b32_e32 v3, 7, v3
	v_and_b32_e32 v2, 56, v2
	v_and_b32_e32 v4, 62, v1
	s_ashr_i32 s13, s12, 31
	v_add_u32_e32 v165, 0, v5
	s_add_i32 s18, 0, 0x18000
	v_and_b32_e32 v0, 8, v0
	s_lshl_b64 s[12:13], s[12:13], 11
	v_add_u32_e32 v166, s66, v3
	v_lshl_add_u32 v167, v162, 7, 0
	v_add_u32_e32 v168, 0xa000, v165
	v_add_u32_e32 v169, s18, v3
	v_lshlrev_b32_e32 v100, 1, v2
	v_lshlrev_b32_e32 v102, 2, v4
	s_lshl_b32 s19, s14, 1
	v_lshlrev_b32_e32 v104, 1, v6
	v_lshlrev_b32_e32 v106, 1, v0
	v_mbcnt_lo_u32_b32 v184, -1, 0
	v_mbcnt_hi_u32_b32 v184, -1, v184
	v_and_b32_e32 v185, 31, v184
	v_lshrrev_b32_e32 v186, 5, v184
	v_cmp_lt_u32_e64 s[0:1], 15, v185
	v_and_b32_e32 v187, 15, v185
	v_lshlrev_b32_e32 v187, 4, v187
	v_lshl_add_u32 v102, v186, 13, v187
	v_lshlrev_b32_e32 v188, 2, v185
	v_lshl_add_u32 v188, v186, 1, v188
	v_and_b32_e32 v189, 7, v188
	v_xor_b32_e32 v189, s33, v189
	v_lshlrev_b32_e32 v189, 4, v189
	v_lshl_add_u32 v164, v188, 7, v189
	v_add_u32_e32 v188, 1, v188
	v_and_b32_e32 v189, 7, v188
	v_xor_b32_e32 v189, s33, v189
	v_lshlrev_b32_e32 v189, 4, v189
	v_lshl_add_u32 v163, v188, 7, v189
	s_branch .LBB0_1000

.LBB0_1000:
	s_ashr_i32 s2, s16, 31
	s_lshr_b32 s2, s2, 26
	s_add_i32 s2, s16, s2
	s_ashr_i32 s14, s2, 6
	s_andn2_b32 s2, s2, 63
	s_sub_i32 s2, s16, s2
	s_lshl_b32 s14, s14, 3
	s_and_b32 s15, s2, 7
	s_or_b32 s21, s14, s15
	v_cmp_ge_i32_e32 vcc, s21, v158
	s_cbranch_vccnz .LBB0_999
	s_lshl_b32 s14, s21, 2
	s_add_i32 s14, s14, 0
	s_add_i32 s14, s14, 0x20b40
	v_mov_b32_e32 v0, s14
	ds_read_b32 v0, v0
	s_mul_i32 s20, s21, 5
	v_mov_b32_e32 v2, v145
	s_mulk_i32 s21, 0x140
	s_mov_b64 s[14:15], s[4:5]
	v_add3_u32 v144, s21, v159, v2
	s_mov_b64 s[22:23], s[8:9]
	s_mov_b64 s[24:25], s[6:7]
	v_lshlrev_b64 v[4:5], 12, v[144:145]
	v_mov_b32_e32 v101, v145
	v_lshl_add_u64 v[4:5], s[14:15], 0, v[4:5]
	s_lshl_b32 s2, s2, 3
	v_lshl_add_u64 v[108:109], v[4:5], 0, v[100:101]
	v_mov_b32_e32 v3, s25
	v_mov_b32_e32 v4, s23
	s_and_b32 s14, s2, 0xffffffc0
	s_and_b32 s2, s20, 31
	s_waitcnt lgkmcnt(0)
	v_ashrrev_i32_e32 v1, 31, v0
	v_cndmask_b32_e64 v5, v3, v4, s[0:1]
	v_mov_b32_e32 v3, s24
	v_mov_b32_e32 v4, s22
	s_lshl_b32 s36, s2, 7
	v_cndmask_b32_e64 v4, v3, v4, s[0:1]
	v_lshlrev_b64 v[0:1], 22, v[0:1]
	v_lshl_add_u64 v[16:17], v[108:109], 0, s[36:37]
	v_lshl_add_u64 v[0:1], v[4:5], 0, v[0:1]
	v_add_co_u32_e32 v4, vcc, s53, v16
	s_ashr_i32 s15, s14, 31
	s_nop 0
	v_addc_co_u32_e32 v5, vcc, 0, v17, vcc
	v_add_co_u32_e32 v8, vcc, s82, v16
	v_lshl_add_u64 v[0:1], s[14:15], 2, v[0:1]
	v_mov_b32_e32 v103, v145
	v_addc_co_u32_e32 v9, vcc, 0, v17, vcc
	v_lshl_add_u64 v[0:1], v[0:1], 0, v[102:103]
	v_ashrrev_i32_e32 v3, 31, v2
	v_add_co_u32_e32 v12, vcc, s47, v16
	v_lshl_add_u64 v[0:1], v[2:3], 2, v[0:1]
	s_nop 0
	v_addc_co_u32_e32 v13, vcc, 0, v17, vcc
	v_lshl_add_u64 v[110:111], v[0:1], 0, s[12:13]
	global_load_dwordx4 v[0:3], v[16:17], off
	s_nop 0
	global_load_dwordx4 v[4:7], v[4:5], off
	v_add_co_u32_e32 v16, vcc, s49, v16
	s_lshl_b32 s36, s2, 17
	s_nop 0
	v_addc_co_u32_e32 v17, vcc, 0, v17, vcc
	global_load_dwordx4 v[8:11], v[8:9], off
	s_nop 0
	global_load_dwordx4 v[12:15], v[12:13], off
	global_load_dwordx4 v[16:19], v[16:17], off
	v_lshl_add_u64 v[28:29], v[110:111], 0, s[36:37]
	v_add_co_u32_e32 v32, vcc, 0x1000, v28
	s_nop 1
	v_addc_co_u32_e32 v33, vcc, 0, v29, vcc
	global_load_dwordx4 v[20:23], v[28:29], off
	global_load_dwordx4 v[24:27], v[28:29], off offset:2048
	global_load_dwordx4 v[28:31], v[32:33], off
	global_load_dwordx4 v[32:35], v[32:33], off offset:2048
	s_nop 0
	s_nop 0
	s_nop 0
	s_nop 0
	s_nop 0
	s_nop 0
	s_add_i32 s2, s20, 1
	s_and_b32 s2, s2, 31
	s_lshl_b32 s36, s2, 17
	v_lshl_add_u64 v[120:121], v[110:111], 0, s[36:37]
	v_add_co_u32_e32 v124, vcc, 0x1000, v120
	s_nop 1
	v_addc_co_u32_e32 v125, vcc, 0, v121, vcc
	global_load_dwordx4 v[112:115], v[120:121], off
	global_load_dwordx4 v[116:119], v[120:121], off offset:2048
	global_load_dwordx4 v[120:123], v[124:125], off
	global_load_dwordx4 v[124:127], v[124:125], off offset:2048
	v_add_u32_e32 v101, s66, v164
	s_nop 0
	s_lshl_b32 s36, s2, 7
	s_nop 0
	v_add_u32_e32 v103, s66, v163
	s_nop 0
	v_mov_b32_e32 v64, 0
	s_mov_b32 s22, -2
	s_waitcnt vmcnt(0)
	ds_write_b128 v165, v[0:3]
	ds_write_b128 v165, v[4:7] offset:8192
	ds_write_b128 v165, v[8:11] offset:16384
	ds_write_b128 v165, v[12:15] offset:24576
	ds_write_b128 v165, v[16:19] offset:32768
	v_mov_b32_e32 v65, v64
	v_mov_b32_e32 v66, v64
	v_mov_b32_e32 v67, v64
	v_mov_b32_e32 v72, v64
	v_mov_b32_e32 v73, v64
	v_mov_b32_e32 v74, v64
	v_mov_b32_e32 v75, v64
	v_mov_b32_e32 v68, v64
	v_permlane32_swap_b32_e32 v20, v22
	v_permlane32_swap_b32_e32 v21, v23
	v_permlane32_swap_b32_e32 v24, v26
	v_permlane32_swap_b32_e32 v25, v27
	v_permlane32_swap_b32_e32 v28, v30
	v_permlane32_swap_b32_e32 v29, v31
	v_permlane32_swap_b32_e32 v32, v34
	v_permlane32_swap_b32_e32 v33, v35
	v_cvt_pk_bf16_f32 v0, v20, v24
	v_cvt_pk_bf16_f32 v1, v28, v32
	v_cvt_pk_bf16_f32 v2, v22, v26
	v_cvt_pk_bf16_f32 v3, v30, v34
	v_cvt_pk_bf16_f32 v4, v21, v25
	v_cvt_pk_bf16_f32 v5, v29, v33
	v_cvt_pk_bf16_f32 v6, v23, v27
	v_cvt_pk_bf16_f32 v7, v31, v35
	ds_write_b128 v101, v[0:3]
	v_lshl_add_u64 v[0:1], v[108:109], 0, s[36:37]
	v_add_co_u32_e32 v2, vcc, 0x40000, v0
	ds_write_b128 v103, v[4:7]
	s_nop 0
	v_addc_co_u32_e32 v3, vcc, 0, v1, vcc
	global_load_dwordx4 v[80:83], v[0:1], off
	global_load_dwordx4 v[84:87], v[2:3], off
	v_add_co_u32_e32 v2, vcc, s82, v0
	v_mov_b32_e32 v69, v64
	s_nop 0
	v_addc_co_u32_e32 v3, vcc, 0, v1, vcc
	v_add_co_u32_e32 v4, vcc, 0xc0000, v0
	v_mov_b32_e32 v70, v64
	s_nop 0
	v_addc_co_u32_e32 v5, vcc, 0, v1, vcc
	v_add_co_u32_e32 v0, vcc, 0x100000, v0
	global_load_dwordx4 v[88:91], v[2:3], off
	global_load_dwordx4 v[92:95], v[4:5], off
	v_addc_co_u32_e32 v1, vcc, 0, v1, vcc
	global_load_dwordx4 v[96:99], v[0:1], off
	v_mov_b32_e32 v71, v64
	v_mov_b32_e32 v76, v64
	v_mov_b32_e32 v77, v64
	v_mov_b32_e32 v78, v64
	v_mov_b32_e32 v79, v64
	v_mov_b32_e32 v56, v64
	v_mov_b32_e32 v57, v64
	v_mov_b32_e32 v58, v64
	v_mov_b32_e32 v59, v64
	v_mov_b32_e32 v48, v64
	v_mov_b32_e32 v49, v64
	v_mov_b32_e32 v50, v64
	v_mov_b32_e32 v51, v64
	v_mov_b32_e32 v60, v64
	v_mov_b32_e32 v61, v64
	v_mov_b32_e32 v62, v64
	v_mov_b32_e32 v63, v64
	v_mov_b32_e32 v52, v64
	v_mov_b32_e32 v53, v64
	v_mov_b32_e32 v54, v64
	v_mov_b32_e32 v55, v64
	v_mov_b32_e32 v40, v64
	v_mov_b32_e32 v41, v64
	v_mov_b32_e32 v42, v64
	v_mov_b32_e32 v43, v64
	v_mov_b32_e32 v32, v64
	v_mov_b32_e32 v33, v64
	v_mov_b32_e32 v34, v64
	v_mov_b32_e32 v35, v64
	v_mov_b32_e32 v44, v64
	v_mov_b32_e32 v45, v64
	v_mov_b32_e32 v46, v64
	v_mov_b32_e32 v47, v64
	v_mov_b32_e32 v36, v64
	v_mov_b32_e32 v37, v64
	v_mov_b32_e32 v38, v64
	v_mov_b32_e32 v39, v64
	v_mov_b32_e32 v24, v64
	v_mov_b32_e32 v25, v64
	v_mov_b32_e32 v26, v64
	v_mov_b32_e32 v27, v64
	v_mov_b32_e32 v16, v64
	v_mov_b32_e32 v17, v64
	v_mov_b32_e32 v18, v64
	v_mov_b32_e32 v19, v64
	v_mov_b32_e32 v28, v64
	v_mov_b32_e32 v29, v64
	v_mov_b32_e32 v30, v64
	v_mov_b32_e32 v31, v64
	v_mov_b32_e32 v20, v64
	v_mov_b32_e32 v21, v64
	v_mov_b32_e32 v22, v64
	v_mov_b32_e32 v23, v64
	v_mov_b32_e32 v8, v64
	v_mov_b32_e32 v9, v64
	v_mov_b32_e32 v10, v64
	v_mov_b32_e32 v11, v64
	v_mov_b32_e32 v0, v64
	v_mov_b32_e32 v1, v64
	v_mov_b32_e32 v2, v64
	v_mov_b32_e32 v3, v64
	v_mov_b32_e32 v12, v64
	v_mov_b32_e32 v13, v64
	v_mov_b32_e32 v14, v64
	v_mov_b32_e32 v15, v64
	v_mov_b32_e32 v4, v64
	v_mov_b32_e32 v5, v64
	v_mov_b32_e32 v6, v64
	v_mov_b32_e32 v7, v64
	s_waitcnt lgkmcnt(0)
	s_barrier
.LBB0_1002:
	s_add_i32 s2, s20, s22
	s_add_i32 s23, s2, 4
	s_and_b32 s23, s23, 31
	s_lshl_b32 s36, s23, 17
	v_add_u32_e32 v105, v166, v161
	s_nop 0
	s_nop 1
	v_lshl_add_u64 v[136:137], v[110:111], 0, s[36:37]
	v_add_co_u32_e32 v140, vcc, 0x1000, v136
	s_nop 1
	v_addc_co_u32_e32 v141, vcc, 0, v137, vcc
	global_load_dwordx4 v[128:131], v[136:137], off
	global_load_dwordx4 v[132:135], v[136:137], off offset:2048
	global_load_dwordx4 v[136:139], v[140:141], off
	global_load_dwordx4 v[140:143], v[140:141], off offset:2048
	ds_read_b128 v[146:149], v105
	ds_read_b128 v[150:153], v105 offset:2048
	ds_read_b128 v[154:157], v105 offset:8192
	ds_read_b128 v[170:173], v105 offset:10240
	v_add_u32_e32 v105, v167, v161
	ds_read_b128 v[174:177], v105
	ds_read_b128 v[178:181], v105 offset:2048
	s_setprio 1
	s_waitcnt lgkmcnt(1)
	v_mfma_f32_16x16x32_bf16 v[76:79], v[146:149], v[174:177], v[76:79]
	v_mfma_f32_16x16x32_bf16 v[68:71], v[150:153], v[174:177], v[68:71]
	v_mfma_f32_16x16x32_bf16 v[72:75], v[154:157], v[174:177], v[72:75]
	v_mfma_f32_16x16x32_bf16 v[64:67], v[170:173], v[174:177], v[64:67]
	s_setprio 0
	ds_read_b128 v[174:177], v105 offset:4096
	s_setprio 1
	s_waitcnt lgkmcnt(1)
	v_mfma_f32_16x16x32_bf16 v[56:59], v[146:149], v[178:181], v[56:59]
	v_mfma_f32_16x16x32_bf16 v[48:51], v[150:153], v[178:181], v[48:51]
	v_mfma_f32_16x16x32_bf16 v[60:63], v[154:157], v[178:181], v[60:63]
	v_mfma_f32_16x16x32_bf16 v[52:55], v[170:173], v[178:181], v[52:55]
	s_setprio 0
	ds_read_b128 v[178:181], v105 offset:6144
	s_setprio 1
	s_waitcnt lgkmcnt(1)
	v_mfma_f32_16x16x32_bf16 v[40:43], v[146:149], v[174:177], v[40:43]
	v_mfma_f32_16x16x32_bf16 v[32:35], v[150:153], v[174:177], v[32:35]
	v_mfma_f32_16x16x32_bf16 v[44:47], v[154:157], v[174:177], v[44:47]
	v_mfma_f32_16x16x32_bf16 v[36:39], v[170:173], v[174:177], v[36:39]
	s_setprio 0
	ds_read_b128 v[174:177], v105 offset:8192
	s_setprio 1
	s_waitcnt lgkmcnt(1)
	v_mfma_f32_16x16x32_bf16 v[24:27], v[146:149], v[178:181], v[24:27]
	v_mfma_f32_16x16x32_bf16 v[16:19], v[150:153], v[178:181], v[16:19]
	v_mfma_f32_16x16x32_bf16 v[28:31], v[154:157], v[178:181], v[28:31]
	v_mfma_f32_16x16x32_bf16 v[20:23], v[170:173], v[178:181], v[20:23]
	s_setprio 0
	s_setprio 1
	s_waitcnt lgkmcnt(0)
	v_mfma_f32_16x16x32_bf16 v[8:11], v[146:149], v[174:177], v[8:11]
	v_mfma_f32_16x16x32_bf16 v[0:3], v[150:153], v[174:177], v[0:3]
	v_mfma_f32_16x16x32_bf16 v[12:15], v[154:157], v[174:177], v[12:15]
	v_mfma_f32_16x16x32_bf16 v[4:7], v[170:173], v[174:177], v[4:7]
	s_setprio 0
	v_add_u32_e32 v107, v166, v160
	ds_read_b128 v[146:149], v107
	ds_read_b128 v[150:153], v107 offset:2048
	ds_read_b128 v[154:157], v107 offset:8192
	ds_read_b128 v[170:173], v107 offset:10240
	v_add_u32_e32 v107, v167, v160
	ds_read_b128 v[174:177], v107
	ds_read_b128 v[178:181], v107 offset:2048
	s_setprio 1
	s_waitcnt lgkmcnt(1)
	v_mfma_f32_16x16x32_bf16 v[76:79], v[146:149], v[174:177], v[76:79]
	v_mfma_f32_16x16x32_bf16 v[68:71], v[150:153], v[174:177], v[68:71]
	v_mfma_f32_16x16x32_bf16 v[72:75], v[154:157], v[174:177], v[72:75]
	v_mfma_f32_16x16x32_bf16 v[64:67], v[170:173], v[174:177], v[64:67]
	s_setprio 0
	ds_read_b128 v[174:177], v107 offset:4096
	s_setprio 1
	s_waitcnt lgkmcnt(1)
	v_mfma_f32_16x16x32_bf16 v[56:59], v[146:149], v[178:181], v[56:59]
	v_mfma_f32_16x16x32_bf16 v[48:51], v[150:153], v[178:181], v[48:51]
	v_mfma_f32_16x16x32_bf16 v[60:63], v[154:157], v[178:181], v[60:63]
	v_mfma_f32_16x16x32_bf16 v[52:55], v[170:173], v[178:181], v[52:55]
	s_setprio 0
	ds_read_b128 v[178:181], v107 offset:6144
	s_setprio 1
	s_waitcnt lgkmcnt(1)
	v_mfma_f32_16x16x32_bf16 v[40:43], v[146:149], v[174:177], v[40:43]
	v_mfma_f32_16x16x32_bf16 v[32:35], v[150:153], v[174:177], v[32:35]
	v_mfma_f32_16x16x32_bf16 v[44:47], v[154:157], v[174:177], v[44:47]
	v_mfma_f32_16x16x32_bf16 v[36:39], v[170:173], v[174:177], v[36:39]
	s_setprio 0
	ds_read_b128 v[174:177], v107 offset:8192
	s_setprio 1
	s_waitcnt lgkmcnt(1)
	v_mfma_f32_16x16x32_bf16 v[24:27], v[146:149], v[178:181], v[24:27]
	v_mfma_f32_16x16x32_bf16 v[16:19], v[150:153], v[178:181], v[16:19]
	v_mfma_f32_16x16x32_bf16 v[28:31], v[154:157], v[178:181], v[28:31]
	v_mfma_f32_16x16x32_bf16 v[20:23], v[170:173], v[178:181], v[20:23]
	s_setprio 0
	s_setprio 1
	s_waitcnt lgkmcnt(0)
	v_mfma_f32_16x16x32_bf16 v[8:11], v[146:149], v[174:177], v[8:11]
	v_mfma_f32_16x16x32_bf16 v[0:3], v[150:153], v[174:177], v[0:3]
	v_mfma_f32_16x16x32_bf16 v[12:15], v[154:157], v[174:177], v[12:15]
	v_mfma_f32_16x16x32_bf16 v[4:7], v[170:173], v[174:177], v[4:7]
	s_setprio 0
	s_waitcnt vmcnt(8)
	ds_write_b128 v165, v[80:83] offset:40960
	s_waitcnt vmcnt(7)
	ds_write_b128 v165, v[84:87] offset:49152
	s_waitcnt vmcnt(6)
	ds_write_b128 v165, v[88:91] offset:57344
	s_waitcnt vmcnt(5)
	ds_write_b128 v168, v[92:95] offset:24576
	s_waitcnt vmcnt(4)
	ds_write_b128 v168, v[96:99] offset:32768
	v_permlane32_swap_b32_e32 v112, v114
	v_permlane32_swap_b32_e32 v113, v115
	v_permlane32_swap_b32_e32 v116, v118
	v_permlane32_swap_b32_e32 v117, v119
	v_permlane32_swap_b32_e32 v120, v122
	v_permlane32_swap_b32_e32 v121, v123
	v_permlane32_swap_b32_e32 v124, v126
	v_permlane32_swap_b32_e32 v125, v127
	v_cvt_pk_bf16_f32 v80, v112, v116
	v_cvt_pk_bf16_f32 v81, v120, v124
	v_cvt_pk_bf16_f32 v82, v114, v118
	v_cvt_pk_bf16_f32 v83, v122, v126
	v_cvt_pk_bf16_f32 v84, v113, v117
	v_cvt_pk_bf16_f32 v85, v121, v125
	v_cvt_pk_bf16_f32 v86, v115, v119
	v_cvt_pk_bf16_f32 v87, v123, v127
	v_add_u32_e32 v88, s18, v164
	s_lshl_b32 s36, s23, 7
	v_add_u32_e32 v89, s18, v163
	ds_write_b128 v88, v[80:83]
	ds_write_b128 v89, v[84:87]
	v_lshl_add_u64 v[80:81], v[108:109], 0, s[36:37]
	v_add_co_u32_e32 v84, vcc, s53, v80
	s_add_i32 s2, s2, 5
	s_nop 0
	v_addc_co_u32_e32 v85, vcc, 0, v81, vcc
	v_add_co_u32_e32 v88, vcc, s82, v80
	s_and_b32 s2, s2, 31
	s_nop 0
	v_addc_co_u32_e32 v89, vcc, 0, v81, vcc
	v_add_co_u32_e32 v92, vcc, s47, v80
	s_lshl_b32 s36, s2, 17
	s_nop 0
	v_addc_co_u32_e32 v93, vcc, 0, v81, vcc
	v_add_co_u32_e32 v96, vcc, s49, v80
	s_nop 0
	v_addc_co_u32_e32 v97, vcc, 0, v81, vcc
	global_load_dwordx4 v[80:83], v[80:81], off
	s_nop 0
	global_load_dwordx4 v[84:87], v[84:85], off
	s_nop 0
	global_load_dwordx4 v[88:91], v[88:89], off
	s_nop 0
	global_load_dwordx4 v[92:95], v[92:93], off
	s_nop 0
	global_load_dwordx4 v[96:99], v[96:97], off
	v_lshl_add_u64 v[120:121], v[110:111], 0, s[36:37]
	v_add_co_u32_e32 v124, vcc, 0x1000, v120
	s_nop 1
	v_addc_co_u32_e32 v125, vcc, 0, v121, vcc
	s_waitcnt lgkmcnt(0)
	s_nop 0
	s_barrier
	global_load_dwordx4 v[112:115], v[120:121], off
	global_load_dwordx4 v[116:119], v[120:121], off offset:2048
	global_load_dwordx4 v[120:123], v[124:125], off
	global_load_dwordx4 v[124:127], v[124:125], off offset:2048
	v_add_u32_e32 v144, v169, v161
	ds_read_b128 v[146:149], v144
	ds_read_b128 v[150:153], v144 offset:2048
	ds_read_b128 v[154:157], v144 offset:8192
	ds_read_b128 v[170:173], v144 offset:10240
	ds_read_b128 v[174:177], v105 offset:40960
	ds_read_b128 v[178:181], v105 offset:43008
	s_setprio 1
	s_waitcnt lgkmcnt(1)
	v_mfma_f32_16x16x32_bf16 v[76:79], v[146:149], v[174:177], v[76:79]
	v_mfma_f32_16x16x32_bf16 v[68:71], v[150:153], v[174:177], v[68:71]
	v_mfma_f32_16x16x32_bf16 v[72:75], v[154:157], v[174:177], v[72:75]
	v_mfma_f32_16x16x32_bf16 v[64:67], v[170:173], v[174:177], v[64:67]
	s_setprio 0
	ds_read_b128 v[174:177], v105 offset:45056
	s_setprio 1
	s_waitcnt lgkmcnt(1)
	v_mfma_f32_16x16x32_bf16 v[56:59], v[146:149], v[178:181], v[56:59]
	v_mfma_f32_16x16x32_bf16 v[48:51], v[150:153], v[178:181], v[48:51]
	v_mfma_f32_16x16x32_bf16 v[60:63], v[154:157], v[178:181], v[60:63]
	v_mfma_f32_16x16x32_bf16 v[52:55], v[170:173], v[178:181], v[52:55]
	s_setprio 0
	ds_read_b128 v[178:181], v105 offset:47104
	s_setprio 1
	s_waitcnt lgkmcnt(1)
	v_mfma_f32_16x16x32_bf16 v[40:43], v[146:149], v[174:177], v[40:43]
	v_mfma_f32_16x16x32_bf16 v[32:35], v[150:153], v[174:177], v[32:35]
	v_mfma_f32_16x16x32_bf16 v[44:47], v[154:157], v[174:177], v[44:47]
	v_mfma_f32_16x16x32_bf16 v[36:39], v[170:173], v[174:177], v[36:39]
	s_setprio 0
	ds_read_b128 v[174:177], v105 offset:49152
	s_setprio 1
	s_waitcnt lgkmcnt(1)
	v_mfma_f32_16x16x32_bf16 v[24:27], v[146:149], v[178:181], v[24:27]
	v_mfma_f32_16x16x32_bf16 v[16:19], v[150:153], v[178:181], v[16:19]
	v_mfma_f32_16x16x32_bf16 v[28:31], v[154:157], v[178:181], v[28:31]
	v_mfma_f32_16x16x32_bf16 v[20:23], v[170:173], v[178:181], v[20:23]
	s_setprio 0
	s_setprio 1
	s_waitcnt lgkmcnt(0)
	v_mfma_f32_16x16x32_bf16 v[8:11], v[146:149], v[174:177], v[8:11]
	v_mfma_f32_16x16x32_bf16 v[0:3], v[150:153], v[174:177], v[0:3]
	v_mfma_f32_16x16x32_bf16 v[12:15], v[154:157], v[174:177], v[12:15]
	v_mfma_f32_16x16x32_bf16 v[4:7], v[170:173], v[174:177], v[4:7]
	s_setprio 0
	v_add_u32_e32 v105, v169, v160
	ds_read_b128 v[146:149], v105
	ds_read_b128 v[150:153], v105 offset:2048
	ds_read_b128 v[154:157], v105 offset:8192
	ds_read_b128 v[170:173], v105 offset:10240
	ds_read_b128 v[174:177], v107 offset:40960
	ds_read_b128 v[178:181], v107 offset:43008
	s_setprio 1
	s_waitcnt lgkmcnt(1)
	v_mfma_f32_16x16x32_bf16 v[76:79], v[146:149], v[174:177], v[76:79]
	v_mfma_f32_16x16x32_bf16 v[68:71], v[150:153], v[174:177], v[68:71]
	v_mfma_f32_16x16x32_bf16 v[72:75], v[154:157], v[174:177], v[72:75]
	v_mfma_f32_16x16x32_bf16 v[64:67], v[170:173], v[174:177], v[64:67]
	s_setprio 0
	ds_read_b128 v[174:177], v107 offset:45056
	s_setprio 1
	s_waitcnt lgkmcnt(1)
	v_mfma_f32_16x16x32_bf16 v[56:59], v[146:149], v[178:181], v[56:59]
	v_mfma_f32_16x16x32_bf16 v[48:51], v[150:153], v[178:181], v[48:51]
	v_mfma_f32_16x16x32_bf16 v[60:63], v[154:157], v[178:181], v[60:63]
	v_mfma_f32_16x16x32_bf16 v[52:55], v[170:173], v[178:181], v[52:55]
	s_setprio 0
	ds_read_b128 v[178:181], v107 offset:47104
	s_setprio 1
	s_waitcnt lgkmcnt(1)
	v_mfma_f32_16x16x32_bf16 v[40:43], v[146:149], v[174:177], v[40:43]
	v_mfma_f32_16x16x32_bf16 v[32:35], v[150:153], v[174:177], v[32:35]
	v_mfma_f32_16x16x32_bf16 v[44:47], v[154:157], v[174:177], v[44:47]
	v_mfma_f32_16x16x32_bf16 v[36:39], v[170:173], v[174:177], v[36:39]
	s_setprio 0
	ds_read_b128 v[174:177], v107 offset:49152
	s_setprio 1
	s_waitcnt lgkmcnt(1)
	v_mfma_f32_16x16x32_bf16 v[24:27], v[146:149], v[178:181], v[24:27]
	v_mfma_f32_16x16x32_bf16 v[16:19], v[150:153], v[178:181], v[16:19]
	v_mfma_f32_16x16x32_bf16 v[28:31], v[154:157], v[178:181], v[28:31]
	v_mfma_f32_16x16x32_bf16 v[20:23], v[170:173], v[178:181], v[20:23]
	s_setprio 0
	s_setprio 1
	s_waitcnt lgkmcnt(0)
	v_mfma_f32_16x16x32_bf16 v[8:11], v[146:149], v[174:177], v[8:11]
	v_mfma_f32_16x16x32_bf16 v[0:3], v[150:153], v[174:177], v[0:3]
	v_mfma_f32_16x16x32_bf16 v[12:15], v[154:157], v[174:177], v[12:15]
	v_mfma_f32_16x16x32_bf16 v[4:7], v[170:173], v[174:177], v[4:7]
	s_setprio 0
	s_lshl_b32 s36, s2, 7
	s_waitcnt vmcnt(8)
	ds_write_b128 v165, v[80:83]
	s_waitcnt vmcnt(7)
	ds_write_b128 v165, v[84:87] offset:8192
	s_waitcnt vmcnt(6)
	ds_write_b128 v165, v[88:91] offset:16384
	s_waitcnt vmcnt(5)
	ds_write_b128 v165, v[92:95] offset:24576
	s_waitcnt vmcnt(4)
	ds_write_b128 v165, v[96:99] offset:32768
	v_permlane32_swap_b32_e32 v128, v130
	v_permlane32_swap_b32_e32 v129, v131
	v_permlane32_swap_b32_e32 v132, v134
	v_permlane32_swap_b32_e32 v133, v135
	v_permlane32_swap_b32_e32 v136, v138
	v_permlane32_swap_b32_e32 v137, v139
	v_permlane32_swap_b32_e32 v140, v142
	v_permlane32_swap_b32_e32 v141, v143
	v_cvt_pk_bf16_f32 v80, v128, v132
	v_cvt_pk_bf16_f32 v81, v136, v140
	v_cvt_pk_bf16_f32 v82, v130, v134
	v_cvt_pk_bf16_f32 v83, v138, v142
	v_cvt_pk_bf16_f32 v84, v129, v133
	v_cvt_pk_bf16_f32 v85, v137, v141
	v_cvt_pk_bf16_f32 v86, v131, v135
	v_cvt_pk_bf16_f32 v87, v139, v143
	v_lshl_add_u64 v[96:97], v[108:109], 0, s[36:37]
	ds_write_b128 v101, v[80:83]
	ds_write_b128 v103, v[84:87]
	v_add_co_u32_e32 v84, vcc, s53, v96
	global_load_dwordx4 v[80:83], v[96:97], off
	s_nop 0
	v_addc_co_u32_e32 v85, vcc, 0, v97, vcc
	v_add_co_u32_e32 v88, vcc, s82, v96
	global_load_dwordx4 v[84:87], v[84:85], off
	s_nop 0
	v_addc_co_u32_e32 v89, vcc, 0, v97, vcc
	v_add_co_u32_e32 v92, vcc, s47, v96
	global_load_dwordx4 v[88:91], v[88:89], off
	s_nop 0
	v_addc_co_u32_e32 v93, vcc, 0, v97, vcc
	global_load_dwordx4 v[92:95], v[92:93], off
	v_add_co_u32_e32 v96, vcc, s49, v96
	s_add_i32 s22, s22, 2
	s_nop 0
	v_addc_co_u32_e32 v97, vcc, 0, v97, vcc
	global_load_dwordx4 v[96:99], v[96:97], off
	s_cmp_gt_u32 s22, 29
	s_waitcnt lgkmcnt(0)
	s_barrier
	s_cbranch_scc0 .LBB0_1002
	s_waitcnt vmcnt(4)
	v_mul_f32_e32 v82, 0xbfb8aa3b, v76
	v_mul_f32_e32 v83, 0xbfb8aa3b, v77
	v_exp_f32_e32 v82, v82
	v_exp_f32_e32 v83, v83
	v_mov_b32_e32 v80, v145
	s_mov_b64 s[22:23], s[10:11]
	v_add_f32_e32 v82, 1.0, v82
	v_add_f32_e32 v83, 1.0, v83
	v_rcp_f32_e32 v82, v82
	v_rcp_f32_e32 v83, v83
	s_mov_b64 s[24:25], 0
	s_lshl_b64 s[14:15], s[14:15], 1
	v_pk_mul_f32 v[76:77], v[76:77], v[82:83]
	s_add_u32 s2, s22, s14
	v_pk_mul_f32 v[72:73], v[72:73], v[76:77]
	v_mul_f32_e32 v76, 0xbfb8aa3b, v78
	v_mul_f32_e32 v77, 0xbfb8aa3b, v79
	v_exp_f32_e32 v76, v76
	v_exp_f32_e32 v77, v77
	v_cvt_pk_bf16_f32 v72, v72, v73
	s_addc_u32 s15, s23, s15
	v_add_f32_e32 v76, 1.0, v76
	v_add_f32_e32 v77, 1.0, v77
	v_rcp_f32_e32 v76, v76
	v_rcp_f32_e32 v77, v77
	s_add_u32 s14, s2, s19
	s_addc_u32 s15, s15, 0
	v_mov_b32_e32 v105, v145
	v_pk_mul_f32 v[76:77], v[78:79], v[76:77]
	v_add3_u32 v144, s21, v162, v80
	v_pk_mul_f32 v[74:75], v[74:75], v[76:77]
	v_lshl_add_u64 v[80:81], s[14:15], 0, v[104:105]
	v_cvt_pk_bf16_f32 v73, v74, v75
	v_mul_f32_e32 v74, 0xbfb8aa3b, v68
	v_mul_f32_e32 v75, 0xbfb8aa3b, v69
	v_exp_f32_e32 v74, v74
	v_exp_f32_e32 v75, v75
	v_mov_b32_e32 v107, v145
	v_lshl_add_u64 v[80:81], v[80:81], 0, v[106:107]
	v_add_f32_e32 v74, 1.0, v74
	v_add_f32_e32 v75, 1.0, v75
	v_rcp_f32_e32 v74, v74
	v_rcp_f32_e32 v75, v75
	s_nop 0
	v_pk_mul_f32 v[68:69], v[68:69], v[74:75]
	s_nop 0
	v_pk_mul_f32 v[64:65], v[64:65], v[68:69]
	v_mul_f32_e32 v68, 0xbfb8aa3b, v70
	v_mul_f32_e32 v69, 0xbfb8aa3b, v71
	v_exp_f32_e32 v68, v68
	v_exp_f32_e32 v69, v69
	v_cvt_pk_bf16_f32 v74, v64, v65
	v_lshlrev_b64 v[64:65], 10, v[144:145]
	v_add_f32_e32 v68, 1.0, v68
	v_add_f32_e32 v69, 1.0, v69
	v_rcp_f32_e32 v68, v68
	v_rcp_f32_e32 v69, v69
	v_permlane16_swap_b32_e32 v72, v74
	v_lshl_add_u64 v[64:65], v[80:81], 0, v[64:65]
	v_pk_mul_f32 v[68:69], v[70:71], v[68:69]
	s_nop 0
	v_pk_mul_f32 v[66:67], v[66:67], v[68:69]
	s_nop 0
	v_cvt_pk_bf16_f32 v75, v66, v67
	s_nop 1
	v_permlane16_swap_b32_e32 v73, v75
	global_store_dwordx4 v[64:65], v[72:75], off
	v_mul_f32_e32 v65, 0xbfb8aa3b, v56
	v_exp_f32_e32 v65, v65
	v_add_u32_e32 v64, 16, v144
	v_add_f32_e32 v65, 1.0, v65
	v_rcp_f32_e32 v66, v65
	v_mul_f32_e32 v65, 0xbfb8aa3b, v57
	v_exp_f32_e32 v65, v65
	s_nop 0
	v_add_f32_e32 v65, 1.0, v65
	v_rcp_f32_e32 v67, v65
	v_mov_b32_e32 v65, v145
	v_pk_mul_f32 v[56:57], v[56:57], v[66:67]
	s_nop 0
	v_pk_mul_f32 v[56:57], v[60:61], v[56:57]
	v_mul_f32_e32 v60, 0xbfb8aa3b, v58
	v_mul_f32_e32 v61, 0xbfb8aa3b, v59
	v_exp_f32_e32 v60, v60
	v_exp_f32_e32 v61, v61
	v_cvt_pk_bf16_f32 v56, v56, v57
	v_add_f32_e32 v60, 1.0, v60
	v_add_f32_e32 v61, 1.0, v61
	v_rcp_f32_e32 v60, v60
	v_rcp_f32_e32 v61, v61
	s_nop 0
	v_pk_mul_f32 v[58:59], v[58:59], v[60:61]
	s_nop 0
	v_pk_mul_f32 v[58:59], v[62:63], v[58:59]
	s_nop 0
	v_cvt_pk_bf16_f32 v57, v58, v59
	v_mul_f32_e32 v58, 0xbfb8aa3b, v48
	v_mul_f32_e32 v59, 0xbfb8aa3b, v49
	v_exp_f32_e32 v58, v58
	v_exp_f32_e32 v59, v59
	v_add_f32_e32 v58, 1.0, v58
	v_add_f32_e32 v59, 1.0, v59
	v_rcp_f32_e32 v58, v58
	v_rcp_f32_e32 v59, v59
	s_nop 0
	v_pk_mul_f32 v[48:49], v[48:49], v[58:59]
	s_nop 0
	v_pk_mul_f32 v[48:49], v[52:53], v[48:49]
	v_mul_f32_e32 v52, 0xbfb8aa3b, v50
	v_mul_f32_e32 v53, 0xbfb8aa3b, v51
	v_exp_f32_e32 v52, v52
	v_exp_f32_e32 v53, v53
	v_cvt_pk_bf16_f32 v58, v48, v49
	v_lshlrev_b64 v[48:49], 10, v[64:65]
	v_add_f32_e32 v52, 1.0, v52
	v_add_f32_e32 v53, 1.0, v53
	v_rcp_f32_e32 v52, v52
	v_rcp_f32_e32 v53, v53
	v_permlane16_swap_b32_e32 v56, v58
	v_lshl_add_u64 v[48:49], v[80:81], 0, v[48:49]
	v_pk_mul_f32 v[50:51], v[50:51], v[52:53]
	s_nop 0
	v_pk_mul_f32 v[50:51], v[54:55], v[50:51]
	s_nop 0
	v_cvt_pk_bf16_f32 v59, v50, v51
	s_nop 1
	v_permlane16_swap_b32_e32 v57, v59
	global_store_dwordx4 v[48:49], v[56:59], off
	v_mul_f32_e32 v49, 0xbfb8aa3b, v40
	v_exp_f32_e32 v49, v49
	v_add_u32_e32 v48, 32, v144
	v_add_f32_e32 v49, 1.0, v49
	v_rcp_f32_e32 v50, v49
	v_mul_f32_e32 v49, 0xbfb8aa3b, v41
	v_exp_f32_e32 v49, v49
	s_nop 0
	v_add_f32_e32 v49, 1.0, v49
	v_rcp_f32_e32 v51, v49
	v_mov_b32_e32 v49, v145
	v_pk_mul_f32 v[40:41], v[40:41], v[50:51]
	s_nop 0
	v_pk_mul_f32 v[40:41], v[44:45], v[40:41]
	v_mul_f32_e32 v44, 0xbfb8aa3b, v42
	v_mul_f32_e32 v45, 0xbfb8aa3b, v43
	v_exp_f32_e32 v44, v44
	v_exp_f32_e32 v45, v45
	v_cvt_pk_bf16_f32 v40, v40, v41
	v_add_f32_e32 v44, 1.0, v44
	v_add_f32_e32 v45, 1.0, v45
	v_rcp_f32_e32 v44, v44
	v_rcp_f32_e32 v45, v45
	s_nop 0
	v_pk_mul_f32 v[42:43], v[42:43], v[44:45]
	s_nop 0
	v_pk_mul_f32 v[42:43], v[46:47], v[42:43]
	s_nop 0
	v_cvt_pk_bf16_f32 v41, v42, v43
	v_mul_f32_e32 v42, 0xbfb8aa3b, v32
	v_mul_f32_e32 v43, 0xbfb8aa3b, v33
	v_exp_f32_e32 v42, v42
	v_exp_f32_e32 v43, v43
	v_add_f32_e32 v42, 1.0, v42
	v_add_f32_e32 v43, 1.0, v43
	v_rcp_f32_e32 v42, v42
	v_rcp_f32_e32 v43, v43
	s_nop 0
	v_pk_mul_f32 v[32:33], v[32:33], v[42:43]
	s_nop 0
	v_pk_mul_f32 v[32:33], v[36:37], v[32:33]
	v_mul_f32_e32 v36, 0xbfb8aa3b, v34
	v_mul_f32_e32 v37, 0xbfb8aa3b, v35
	v_exp_f32_e32 v36, v36
	v_exp_f32_e32 v37, v37
	v_cvt_pk_bf16_f32 v42, v32, v33
	v_lshlrev_b64 v[32:33], 10, v[48:49]
	v_add_f32_e32 v36, 1.0, v36
	v_add_f32_e32 v37, 1.0, v37
	v_rcp_f32_e32 v36, v36
	v_rcp_f32_e32 v37, v37
	v_permlane16_swap_b32_e32 v40, v42
	v_lshl_add_u64 v[32:33], v[80:81], 0, v[32:33]
	v_pk_mul_f32 v[34:35], v[34:35], v[36:37]
	s_nop 0
	v_pk_mul_f32 v[34:35], v[38:39], v[34:35]
	s_nop 0
	v_cvt_pk_bf16_f32 v43, v34, v35
	s_nop 1
	v_permlane16_swap_b32_e32 v41, v43
	global_store_dwordx4 v[32:33], v[40:43], off
	v_mul_f32_e32 v33, 0xbfb8aa3b, v24
	v_exp_f32_e32 v33, v33
	v_add_u32_e32 v32, 48, v144
	v_add_u32_e32 v144, 64, v144
	v_add_f32_e32 v33, 1.0, v33
	v_rcp_f32_e32 v34, v33
	v_mul_f32_e32 v33, 0xbfb8aa3b, v25
	v_exp_f32_e32 v33, v33
	s_nop 0
	v_add_f32_e32 v33, 1.0, v33
	v_rcp_f32_e32 v35, v33
	v_mov_b32_e32 v33, v145
	v_pk_mul_f32 v[24:25], v[24:25], v[34:35]
	s_nop 0
	v_pk_mul_f32 v[24:25], v[28:29], v[24:25]
	v_mul_f32_e32 v28, 0xbfb8aa3b, v26
	v_mul_f32_e32 v29, 0xbfb8aa3b, v27
	v_exp_f32_e32 v28, v28
	v_exp_f32_e32 v29, v29
	v_cvt_pk_bf16_f32 v24, v24, v25
	v_add_f32_e32 v28, 1.0, v28
	v_add_f32_e32 v29, 1.0, v29
	v_rcp_f32_e32 v28, v28
	v_rcp_f32_e32 v29, v29
	s_nop 0
	v_pk_mul_f32 v[26:27], v[26:27], v[28:29]
	s_nop 0
	v_pk_mul_f32 v[26:27], v[30:31], v[26:27]
	s_nop 0
	v_cvt_pk_bf16_f32 v25, v26, v27
	v_mul_f32_e32 v26, 0xbfb8aa3b, v16
	v_mul_f32_e32 v27, 0xbfb8aa3b, v17
	v_exp_f32_e32 v26, v26
	v_exp_f32_e32 v27, v27
	v_add_f32_e32 v26, 1.0, v26
	v_add_f32_e32 v27, 1.0, v27
	v_rcp_f32_e32 v26, v26
	v_rcp_f32_e32 v27, v27
	s_nop 0
	v_pk_mul_f32 v[16:17], v[16:17], v[26:27]
	s_nop 0
	v_pk_mul_f32 v[16:17], v[20:21], v[16:17]
	v_mul_f32_e32 v20, 0xbfb8aa3b, v18
	v_mul_f32_e32 v21, 0xbfb8aa3b, v19
	v_exp_f32_e32 v20, v20
	v_exp_f32_e32 v21, v21
	v_cvt_pk_bf16_f32 v26, v16, v17
	v_lshlrev_b64 v[16:17], 10, v[32:33]
	v_add_f32_e32 v20, 1.0, v20
	v_add_f32_e32 v21, 1.0, v21
	v_rcp_f32_e32 v20, v20
	v_rcp_f32_e32 v21, v21
	v_permlane16_swap_b32_e32 v24, v26
	v_lshl_add_u64 v[16:17], v[80:81], 0, v[16:17]
	v_pk_mul_f32 v[18:19], v[18:19], v[20:21]
	s_nop 0
	v_pk_mul_f32 v[18:19], v[22:23], v[18:19]
	s_nop 0
	v_cvt_pk_bf16_f32 v27, v18, v19
	s_nop 1
	v_permlane16_swap_b32_e32 v25, v27
	global_store_dwordx4 v[16:17], v[24:27], off
	v_mul_f32_e32 v16, 0xbfb8aa3b, v8
	v_mul_f32_e32 v17, 0xbfb8aa3b, v9
	v_exp_f32_e32 v16, v16
	v_exp_f32_e32 v17, v17
	v_add_f32_e32 v16, 1.0, v16
	v_add_f32_e32 v17, 1.0, v17
	v_rcp_f32_e32 v16, v16
	v_rcp_f32_e32 v17, v17
	s_nop 0
	v_pk_mul_f32 v[8:9], v[8:9], v[16:17]
	s_nop 0
	v_pk_mul_f32 v[8:9], v[12:13], v[8:9]
	v_mul_f32_e32 v12, 0xbfb8aa3b, v10
	v_mul_f32_e32 v13, 0xbfb8aa3b, v11
	v_exp_f32_e32 v12, v12
	v_exp_f32_e32 v13, v13
	v_cvt_pk_bf16_f32 v8, v8, v9
	v_add_f32_e32 v12, 1.0, v12
	v_add_f32_e32 v13, 1.0, v13
	v_rcp_f32_e32 v12, v12
	v_rcp_f32_e32 v13, v13
	s_nop 0
	v_pk_mul_f32 v[10:11], v[10:11], v[12:13]
	s_nop 0
	v_pk_mul_f32 v[10:11], v[14:15], v[10:11]
	s_nop 0
	v_cvt_pk_bf16_f32 v9, v10, v11
	v_mul_f32_e32 v10, 0xbfb8aa3b, v0
	v_mul_f32_e32 v11, 0xbfb8aa3b, v1
	v_exp_f32_e32 v10, v10
	v_exp_f32_e32 v11, v11
	v_add_f32_e32 v10, 1.0, v10
	v_add_f32_e32 v11, 1.0, v11
	v_rcp_f32_e32 v10, v10
	v_rcp_f32_e32 v11, v11
	s_nop 0
	v_pk_mul_f32 v[0:1], v[0:1], v[10:11]
	s_nop 0
	v_pk_mul_f32 v[0:1], v[4:5], v[0:1]
	v_mul_f32_e32 v4, 0xbfb8aa3b, v2
	v_mul_f32_e32 v5, 0xbfb8aa3b, v3
	v_exp_f32_e32 v4, v4
	v_exp_f32_e32 v5, v5
	v_cvt_pk_bf16_f32 v10, v0, v1
	v_lshlrev_b64 v[0:1], 10, v[144:145]
	v_add_f32_e32 v4, 1.0, v4
	v_add_f32_e32 v5, 1.0, v5
	v_rcp_f32_e32 v4, v4
	v_rcp_f32_e32 v5, v5
	v_permlane16_swap_b32_e32 v8, v10
	v_lshl_add_u64 v[0:1], v[80:81], 0, v[0:1]
	v_pk_mul_f32 v[2:3], v[2:3], v[4:5]
	s_nop 0
	v_pk_mul_f32 v[2:3], v[6:7], v[2:3]
	s_nop 0
	v_cvt_pk_bf16_f32 v11, v2, v3
	s_nop 1
	v_permlane16_swap_b32_e32 v9, v11
	global_store_dwordx4 v[0:1], v[8:11], off
	s_branch .LBB0_999

.LBB0_1048:
	s_or_b64 exec, exec, s[64:65]
	s_mov_b32 s0, s37
	s_waitcnt lgkmcnt(0)
	s_barrier
	s_mov_b32 s1, s33
	v_mbcnt_lo_u32_b32 v0, -1, s0
	v_mbcnt_hi_u32_b32 v0, -1, v0
	v_lshl_or_b32 v0, s1, 6, v0
	v_readlane_b32 s0, v254, 0
	s_mov_b32 s16, s0
	s_mov_b32 s0, s37
	s_add_i32 s0, s0, 0x20120
	v_mov_b32_e32 v1, s0
	s_mov_b32 s0, 0
	ds_read_b64 v[2:3], v1
	s_add_i32 s0, s0, 0x200f0
	v_mov_b32_e32 v1, s0
	s_mov_b32 s4, s60
	s_mov_b32 s5, 0
	ds_read_b64 v[4:5], v1
	s_add_i32 s5, s5, 0x20120
	v_readlane_b32 s1, v254, 1
	v_mov_b32_e32 v1, s5
	s_mov_b32 s5, 0
	s_waitcnt lgkmcnt(0)
	v_readfirstlane_b32 s1, v3
	v_readfirstlane_b32 s0, v2
	ds_read_b64 v[2:3], v1
	s_add_i32 s5, s5, 0x20120
	v_mov_b32_e32 v1, s5
	v_readlane_b32 s5, v255, 10
	v_readfirstlane_b32 s2, v5
	v_readfirstlane_b32 s6, v4
	ds_read_b64 v[4:5], v1
	v_mov_b32_e32 v1, s5
	ds_read_b32 v158, v1
	s_waitcnt lgkmcnt(0)
	v_readfirstlane_b32 s7, v3
	v_readfirstlane_b32 s11, v2
	v_readfirstlane_b32 s9, v5
	v_readfirstlane_b32 s8, v4
	v_readfirstlane_b32 s5, v158
	s_lshl_b32 s5, s5, 4
	s_addk_i32 s5, 0x70
	s_and_b32 s17, s5, 0xffffff80
	s_cmp_ge_i32 s16, s17
	v_readfirstlane_b32 s10, v0
	s_cbranch_scc1 .LBB0_1055
	s_add_u32 s0, s0, 0x2779fd00
	s_addc_u32 s1, s1, 0
	s_ashr_i32 s5, s4, 31
	s_lshl_b64 s[4:5], s[4:5], 28
	s_add_u32 s4, s6, s4
	s_addc_u32 s5, s2, s5
	s_add_u32 s6, s11, 0x29b9fd00
	s_addc_u32 s7, s7, 0
	s_add_u32 s8, s8, 0x1e76bd00
	s_addc_u32 s9, s9, 0
	s_and_b32 s2, s10, 64
	v_and_b32_e32 v1, 15, v0
	v_or_b32_e32 v2, s2, v1
	s_ashr_i32 s11, s10, 7
	v_lshlrev_b32_e32 v3, 7, v2
	s_mulk_i32 s11, 0x50
	v_bfe_u32 v2, v0, 4, 2
	v_and_b32_e32 v4, 7, v0
	v_or_b32_e32 v160, s11, v1
	v_and_b32_e32 v1, 63, v0
	v_bitop3_b32 v4, v2, v4, 4 bitop3:0x36
	v_bitop3_b32 v2, v2, v0, 7 bitop3:0x78
	v_lshlrev_b32_e32 v162, 4, v2
	v_lshlrev_b32_e32 v2, 1, v1
	v_lshlrev_b32_e32 v161, 4, v4
	s_ashr_i32 s10, s10, 6
	v_or_b32_e32 v4, 1, v2
	v_bitop3_b32 v5, s10, v4, 7 bitop3:0x78
	v_lshlrev_b32_e32 v4, 7, v4
	v_ashrrev_i32_e32 v159, 3, v0
	v_lshl_add_u32 v163, v5, 4, v4
	v_bitop3_b32 v4, s10, v2, 6 bitop3:0x78
	v_lshlrev_b32_e32 v1, 8, v1
	v_lshl_add_u32 v164, v4, 4, v1
	v_xor_b32_e32 v1, v159, v0
	v_lshlrev_b32_e32 v1, 4, v1
	v_lshlrev_b32_e32 v4, 7, v159
	s_movk_i32 s11, 0x70
	v_and_or_b32 v1, v1, s11, v4
	v_lshlrev_b32_e32 v4, 3, v0
	s_lshl_b32 s10, s10, 3
	v_and_b32_e32 v6, 16, v0
	v_lshrrev_b32_e32 v0, 2, v0
	v_and_b32_e32 v4, 56, v4
	s_ashr_i32 s11, s10, 31
	v_add_u32_e32 v165, 0, v1
	s_add_i32 s18, 0, 0x18000
	v_and_b32_e32 v0, 8, v0
	s_lshl_b64 s[10:11], s[10:11], 13
	v_add_u32_e32 v166, s66, v3
	v_lshl_add_u32 v167, v160, 7, 0
	v_add_u32_e32 v168, 0xa000, v165
	v_add_u32_e32 v169, s18, v3
	v_lshlrev_b32_e32 v100, 1, v4
	v_lshlrev_b32_e32 v102, 2, v2
	s_lshl_b32 s19, s2, 1
	v_lshlrev_b32_e32 v104, 1, v6
	v_lshlrev_b32_e32 v106, 1, v0
	v_mbcnt_lo_u32_b32 v184, -1, 0
	v_mbcnt_hi_u32_b32 v184, -1, v184
	v_and_b32_e32 v185, 31, v184
	v_lshrrev_b32_e32 v186, 5, v184
	v_lshlrev_b32_e32 v187, 4, v185
	v_lshl_add_u32 v102, v186, 15, v187
	v_lshlrev_b32_e32 v188, 2, v185
	v_lshl_add_u32 v188, v186, 1, v188
	v_and_b32_e32 v189, 7, v188
	v_xor_b32_e32 v189, s33, v189
	v_lshlrev_b32_e32 v189, 4, v189
	v_lshl_add_u32 v164, v188, 7, v189
	v_add_u32_e32 v188, 1, v188
	v_and_b32_e32 v189, 7, v188
	v_xor_b32_e32 v189, s33, v189
	v_lshlrev_b32_e32 v189, 4, v189
	v_lshl_add_u32 v163, v188, 7, v189
	s_branch .LBB0_1051

.LBB0_1051:
	s_ashr_i32 s2, s16, 31
	s_lshr_b32 s2, s2, 25
	s_add_i32 s2, s16, s2
	s_ashr_i32 s12, s2, 7
	s_and_b32 s2, s2, 0xffffff80
	s_sub_i32 s2, s16, s2
	s_lshl_b32 s12, s12, 3
	s_and_b32 s13, s2, 7
	s_or_b32 s20, s12, s13
	v_cmp_ge_i32_e32 vcc, s20, v158
	s_cbranch_vccnz .LBB0_1050
	s_lshl_b32 s12, s20, 2
	s_add_i32 s12, s12, 0
	s_add_i32 s12, s12, 0x20b40
	v_mov_b32_e32 v0, s12
	v_mov_b32_e32 v2, v145
	s_mulk_i32 s20, 0x140
	ds_read_b32 v0, v0
	s_mov_b64 s[12:13], s[0:1]
	s_mov_b64 s[22:23], 0
	s_mov_b64 s[24:25], s[4:5]
	v_add3_u32 v144, s20, v159, v2
	s_mul_i32 s14, s2, 5
	v_lshlrev_b64 v[4:5], 10, v[144:145]
	s_lshl_b32 s2, s2, 4
	v_lshl_add_u64 v[4:5], s[12:13], 0, v[4:5]
	v_mov_b32_e32 v101, v145
	s_and_b32 s12, s2, 0xffffff80
	s_and_b32 s2, s14, 7
	v_lshl_add_u64 v[108:109], v[4:5], 0, v[100:101]
	s_lshl_b32 s36, s2, 7
	v_lshl_add_u64 v[16:17], v[108:109], 0, s[36:37]
	s_waitcnt lgkmcnt(0)
	v_ashrrev_i32_e32 v1, 31, v0
	v_add_co_u32_e32 v4, vcc, s70, v16
	v_lshlrev_b64 v[0:1], 22, v[0:1]
	s_ashr_i32 s13, s12, 31
	v_addc_co_u32_e32 v5, vcc, 0, v17, vcc
	v_lshl_add_u64 v[0:1], s[24:25], 0, v[0:1]
	s_lshl_b64 s[22:23], s[12:13], 2
	v_add_co_u32_e32 v8, vcc, s83, v16
	v_lshl_add_u64 v[0:1], v[0:1], 0, s[22:23]
	v_mov_b32_e32 v103, v145
	v_addc_co_u32_e32 v9, vcc, 0, v17, vcc
	v_lshl_add_u64 v[0:1], v[0:1], 0, v[102:103]
	v_ashrrev_i32_e32 v3, 31, v2
	v_add_co_u32_e32 v12, vcc, s3, v16
	v_lshl_add_u64 v[0:1], v[2:3], 2, v[0:1]
	s_nop 0
	v_addc_co_u32_e32 v13, vcc, 0, v17, vcc
	v_lshl_add_u64 v[110:111], v[0:1], 0, s[10:11]
	global_load_dwordx4 v[0:3], v[16:17], off
	s_nop 0
	global_load_dwordx4 v[4:7], v[4:5], off
	v_add_co_u32_e32 v16, vcc, s53, v16
	s_lshl_b32 s36, s2, 19
	s_nop 0
	v_addc_co_u32_e32 v17, vcc, 0, v17, vcc
	global_load_dwordx4 v[8:11], v[8:9], off
	s_nop 0
	global_load_dwordx4 v[12:15], v[12:13], off
	global_load_dwordx4 v[16:19], v[16:17], off
	v_lshl_add_u64 v[32:33], v[110:111], 0, s[36:37]
	v_add_co_u32_e32 v34, vcc, 0x2000, v32
	s_nop 1
	v_addc_co_u32_e32 v35, vcc, 0, v33, vcc
	v_add_co_u32_e32 v28, vcc, 0x4000, v32
	s_nop 1
	v_addc_co_u32_e32 v29, vcc, 0, v33, vcc
	v_add_co_u32_e32 v30, vcc, 0x6000, v32
	s_nop 1
	v_addc_co_u32_e32 v31, vcc, 0, v33, vcc
	global_load_dwordx4 v[20:23], v[32:33], off
	global_load_dwordx4 v[24:27], v[34:35], off
	global_load_dwordx4 v[32:35], v[30:31], off
	global_load_dwordx4 v[28:31], v[28:29], off
	s_nop 0
	s_add_i32 s2, s14, 1
	s_nop 0
	s_nop 0
	s_nop 0
	s_nop 0
	s_and_b32 s2, s2, 7
	s_nop 0
	s_lshl_b32 s36, s2, 19
	s_nop 0
	s_nop 0
	s_nop 0
	s_nop 0
	s_nop 0
	v_lshl_add_u64 v[124:125], v[110:111], 0, s[36:37]
	v_add_co_u32_e32 v126, vcc, 0x2000, v124
	s_nop 1
	v_addc_co_u32_e32 v127, vcc, 0, v125, vcc
	v_add_co_u32_e32 v120, vcc, 0x4000, v124
	s_nop 1
	v_addc_co_u32_e32 v121, vcc, 0, v125, vcc
	v_add_co_u32_e32 v122, vcc, 0x6000, v124
	s_nop 1
	v_addc_co_u32_e32 v123, vcc, 0, v125, vcc
	global_load_dwordx4 v[112:115], v[124:125], off
	global_load_dwordx4 v[116:119], v[126:127], off
	global_load_dwordx4 v[124:127], v[122:123], off
	global_load_dwordx4 v[120:123], v[120:121], off
	v_add_u32_e32 v101, s66, v164
	s_nop 0
	s_lshl_b32 s36, s2, 7
	s_nop 0
	v_add_u32_e32 v103, s66, v163
	s_nop 0
	v_mov_b32_e32 v64, 0
	s_nop 0
	s_mov_b32 s15, -2
	s_nop 0
	v_mov_b32_e32 v65, v64
	s_nop 0
	v_mov_b32_e32 v66, v64
	s_nop 0
	s_waitcnt vmcnt(0)
	ds_write_b128 v165, v[0:3]
	ds_write_b128 v165, v[4:7] offset:8192
	ds_write_b128 v165, v[8:11] offset:16384
	ds_write_b128 v165, v[12:15] offset:24576
	ds_write_b128 v165, v[16:19] offset:32768
	v_mov_b32_e32 v67, v64
	v_mov_b32_e32 v68, v64
	v_mov_b32_e32 v69, v64
	v_mov_b32_e32 v70, v64
	v_mov_b32_e32 v71, v64
	v_mov_b32_e32 v72, v64
	v_mov_b32_e32 v73, v64
	v_mov_b32_e32 v74, v64
	v_mov_b32_e32 v75, v64
	v_mov_b32_e32 v76, v64
	v_mov_b32_e32 v77, v64
	v_permlane32_swap_b32_e32 v20, v22
	v_permlane32_swap_b32_e32 v21, v23
	v_permlane32_swap_b32_e32 v24, v26
	v_permlane32_swap_b32_e32 v25, v27
	v_permlane32_swap_b32_e32 v28, v30
	v_permlane32_swap_b32_e32 v29, v31
	v_permlane32_swap_b32_e32 v32, v34
	v_permlane32_swap_b32_e32 v33, v35
	v_cvt_pk_bf16_f32 v0, v20, v24
	v_cvt_pk_bf16_f32 v1, v28, v32
	v_cvt_pk_bf16_f32 v2, v22, v26
	v_cvt_pk_bf16_f32 v3, v30, v34
	v_cvt_pk_bf16_f32 v4, v21, v25
	v_cvt_pk_bf16_f32 v5, v29, v33
	v_cvt_pk_bf16_f32 v6, v23, v27
	v_cvt_pk_bf16_f32 v7, v31, v35
	v_mov_b32_e32 v78, v64
	v_mov_b32_e32 v79, v64
	v_mov_b32_e32 v48, v64
	v_mov_b32_e32 v49, v64
	v_mov_b32_e32 v50, v64
	v_mov_b32_e32 v51, v64
	v_mov_b32_e32 v52, v64
	v_mov_b32_e32 v53, v64
	v_mov_b32_e32 v54, v64
	v_mov_b32_e32 v55, v64
	v_mov_b32_e32 v56, v64
	v_mov_b32_e32 v57, v64
	v_mov_b32_e32 v58, v64
	v_mov_b32_e32 v59, v64
	ds_write_b128 v101, v[0:3]
	v_lshl_add_u64 v[0:1], v[108:109], 0, s[36:37]
	v_add_co_u32_e32 v2, vcc, s70, v0
	ds_write_b128 v103, v[4:7]
	s_nop 0
	v_addc_co_u32_e32 v3, vcc, 0, v1, vcc
	global_load_dwordx4 v[80:83], v[0:1], off
	global_load_dwordx4 v[84:87], v[2:3], off
	v_add_co_u32_e32 v2, vcc, s83, v0
	v_mov_b32_e32 v60, v64
	s_nop 0
	v_addc_co_u32_e32 v3, vcc, 0, v1, vcc
	v_add_co_u32_e32 v4, vcc, 0x30000, v0
	v_mov_b32_e32 v61, v64
	s_nop 0
	v_addc_co_u32_e32 v5, vcc, 0, v1, vcc
	v_add_co_u32_e32 v0, vcc, 0x40000, v0
	global_load_dwordx4 v[88:91], v[2:3], off
	global_load_dwordx4 v[92:95], v[4:5], off
	v_addc_co_u32_e32 v1, vcc, 0, v1, vcc
	global_load_dwordx4 v[96:99], v[0:1], off
	v_mov_b32_e32 v62, v64
	v_mov_b32_e32 v63, v64
	v_mov_b32_e32 v32, v64
	v_mov_b32_e32 v33, v64
	v_mov_b32_e32 v34, v64
	v_mov_b32_e32 v35, v64
	v_mov_b32_e32 v36, v64
	v_mov_b32_e32 v37, v64
	v_mov_b32_e32 v38, v64
	v_mov_b32_e32 v39, v64
	v_mov_b32_e32 v40, v64
	v_mov_b32_e32 v41, v64
	v_mov_b32_e32 v42, v64
	v_mov_b32_e32 v43, v64
	v_mov_b32_e32 v44, v64
	v_mov_b32_e32 v45, v64
	v_mov_b32_e32 v46, v64
	v_mov_b32_e32 v47, v64
	v_mov_b32_e32 v16, v64
	v_mov_b32_e32 v17, v64
	v_mov_b32_e32 v18, v64
	v_mov_b32_e32 v19, v64
	v_mov_b32_e32 v20, v64
	v_mov_b32_e32 v21, v64
	v_mov_b32_e32 v22, v64
	v_mov_b32_e32 v23, v64
	v_mov_b32_e32 v24, v64
	v_mov_b32_e32 v25, v64
	v_mov_b32_e32 v26, v64
	v_mov_b32_e32 v27, v64
	v_mov_b32_e32 v28, v64
	v_mov_b32_e32 v29, v64
	v_mov_b32_e32 v30, v64
	v_mov_b32_e32 v31, v64
	v_mov_b32_e32 v0, v64
	v_mov_b32_e32 v1, v64
	v_mov_b32_e32 v2, v64
	v_mov_b32_e32 v3, v64
	v_mov_b32_e32 v4, v64
	v_mov_b32_e32 v5, v64
	v_mov_b32_e32 v6, v64
	v_mov_b32_e32 v7, v64
	v_mov_b32_e32 v8, v64
	v_mov_b32_e32 v9, v64
	v_mov_b32_e32 v10, v64
	v_mov_b32_e32 v11, v64
	v_mov_b32_e32 v12, v64
	v_mov_b32_e32 v13, v64
	v_mov_b32_e32 v14, v64
	v_mov_b32_e32 v15, v64
	s_waitcnt lgkmcnt(0)
	s_barrier
.LBB0_1053:
	s_add_i32 s2, s14, s15
	s_add_i32 s21, s2, 4
	s_and_b32 s21, s21, 7
	s_lshl_b32 s36, s21, 19
	v_add_u32_e32 v105, v166, v162
	s_nop 0
	s_nop 1
	s_nop 1
	s_nop 1
	s_nop 1
	s_nop 1
	v_lshl_add_u64 v[140:141], v[110:111], 0, s[36:37]
	v_add_co_u32_e32 v142, vcc, 0x2000, v140
	s_nop 1
	v_addc_co_u32_e32 v143, vcc, 0, v141, vcc
	v_add_co_u32_e32 v136, vcc, 0x4000, v140
	s_nop 1
	v_addc_co_u32_e32 v137, vcc, 0, v141, vcc
	v_add_co_u32_e32 v138, vcc, 0x6000, v140
	s_nop 1
	v_addc_co_u32_e32 v139, vcc, 0, v141, vcc
	global_load_dwordx4 v[128:131], v[140:141], off
	global_load_dwordx4 v[132:135], v[142:143], off
	global_load_dwordx4 v[140:143], v[138:139], off
	global_load_dwordx4 v[136:139], v[136:137], off
	ds_read_b128 v[146:149], v105
	ds_read_b128 v[150:153], v105 offset:2048
	ds_read_b128 v[154:157], v105 offset:4096
	ds_read_b128 v[170:173], v105 offset:6144
	v_add_u32_e32 v105, v167, v162
	ds_read_b128 v[174:177], v105
	ds_read_b128 v[178:181], v105 offset:2048
	s_setprio 1
	s_waitcnt lgkmcnt(1)
	v_mfma_f32_16x16x32_bf16 v[76:79], v[146:149], v[174:177], v[76:79]
	v_mfma_f32_16x16x32_bf16 v[72:75], v[150:153], v[174:177], v[72:75]
	v_mfma_f32_16x16x32_bf16 v[68:71], v[154:157], v[174:177], v[68:71]
	v_mfma_f32_16x16x32_bf16 v[64:67], v[170:173], v[174:177], v[64:67]
	s_setprio 0
	ds_read_b128 v[174:177], v105 offset:4096
	s_setprio 1
	s_waitcnt lgkmcnt(1)
	v_mfma_f32_16x16x32_bf16 v[48:51], v[146:149], v[178:181], v[48:51]
	v_mfma_f32_16x16x32_bf16 v[52:55], v[150:153], v[178:181], v[52:55]
	v_mfma_f32_16x16x32_bf16 v[56:59], v[154:157], v[178:181], v[56:59]
	v_mfma_f32_16x16x32_bf16 v[60:63], v[170:173], v[178:181], v[60:63]
	s_setprio 0
	ds_read_b128 v[178:181], v105 offset:6144
	s_setprio 1
	s_waitcnt lgkmcnt(1)
	v_mfma_f32_16x16x32_bf16 v[32:35], v[146:149], v[174:177], v[32:35]
	v_mfma_f32_16x16x32_bf16 v[36:39], v[150:153], v[174:177], v[36:39]
	v_mfma_f32_16x16x32_bf16 v[40:43], v[154:157], v[174:177], v[40:43]
	v_mfma_f32_16x16x32_bf16 v[44:47], v[170:173], v[174:177], v[44:47]
	s_setprio 0
	ds_read_b128 v[174:177], v105 offset:8192
	s_setprio 1
	s_waitcnt lgkmcnt(1)
	v_mfma_f32_16x16x32_bf16 v[16:19], v[146:149], v[178:181], v[16:19]
	v_mfma_f32_16x16x32_bf16 v[20:23], v[150:153], v[178:181], v[20:23]
	v_mfma_f32_16x16x32_bf16 v[24:27], v[154:157], v[178:181], v[24:27]
	v_mfma_f32_16x16x32_bf16 v[28:31], v[170:173], v[178:181], v[28:31]
	s_setprio 0
	s_setprio 1
	s_waitcnt lgkmcnt(0)
	v_mfma_f32_16x16x32_bf16 v[0:3], v[146:149], v[174:177], v[0:3]
	v_mfma_f32_16x16x32_bf16 v[4:7], v[150:153], v[174:177], v[4:7]
	v_mfma_f32_16x16x32_bf16 v[8:11], v[154:157], v[174:177], v[8:11]
	v_mfma_f32_16x16x32_bf16 v[12:15], v[170:173], v[174:177], v[12:15]
	s_setprio 0
	v_add_u32_e32 v107, v166, v161
	ds_read_b128 v[146:149], v107
	ds_read_b128 v[150:153], v107 offset:2048
	ds_read_b128 v[154:157], v107 offset:4096
	ds_read_b128 v[170:173], v107 offset:6144
	v_add_u32_e32 v107, v167, v161
	ds_read_b128 v[174:177], v107
	ds_read_b128 v[178:181], v107 offset:2048
	s_setprio 1
	s_waitcnt lgkmcnt(1)
	v_mfma_f32_16x16x32_bf16 v[76:79], v[146:149], v[174:177], v[76:79]
	v_mfma_f32_16x16x32_bf16 v[72:75], v[150:153], v[174:177], v[72:75]
	v_mfma_f32_16x16x32_bf16 v[68:71], v[154:157], v[174:177], v[68:71]
	v_mfma_f32_16x16x32_bf16 v[64:67], v[170:173], v[174:177], v[64:67]
	s_setprio 0
	ds_read_b128 v[174:177], v107 offset:4096
	s_setprio 1
	s_waitcnt lgkmcnt(1)
	v_mfma_f32_16x16x32_bf16 v[48:51], v[146:149], v[178:181], v[48:51]
	v_mfma_f32_16x16x32_bf16 v[52:55], v[150:153], v[178:181], v[52:55]
	v_mfma_f32_16x16x32_bf16 v[56:59], v[154:157], v[178:181], v[56:59]
	v_mfma_f32_16x16x32_bf16 v[60:63], v[170:173], v[178:181], v[60:63]
	s_setprio 0
	ds_read_b128 v[178:181], v107 offset:6144
	s_setprio 1
	s_waitcnt lgkmcnt(1)
	v_mfma_f32_16x16x32_bf16 v[32:35], v[146:149], v[174:177], v[32:35]
	v_mfma_f32_16x16x32_bf16 v[36:39], v[150:153], v[174:177], v[36:39]
	v_mfma_f32_16x16x32_bf16 v[40:43], v[154:157], v[174:177], v[40:43]
	v_mfma_f32_16x16x32_bf16 v[44:47], v[170:173], v[174:177], v[44:47]
	s_setprio 0
	ds_read_b128 v[174:177], v107 offset:8192
	s_setprio 1
	s_waitcnt lgkmcnt(1)
	v_mfma_f32_16x16x32_bf16 v[16:19], v[146:149], v[178:181], v[16:19]
	v_mfma_f32_16x16x32_bf16 v[20:23], v[150:153], v[178:181], v[20:23]
	v_mfma_f32_16x16x32_bf16 v[24:27], v[154:157], v[178:181], v[24:27]
	v_mfma_f32_16x16x32_bf16 v[28:31], v[170:173], v[178:181], v[28:31]
	s_setprio 0
	s_setprio 1
	s_waitcnt lgkmcnt(0)
	v_mfma_f32_16x16x32_bf16 v[0:3], v[146:149], v[174:177], v[0:3]
	v_mfma_f32_16x16x32_bf16 v[4:7], v[150:153], v[174:177], v[4:7]
	v_mfma_f32_16x16x32_bf16 v[8:11], v[154:157], v[174:177], v[8:11]
	v_mfma_f32_16x16x32_bf16 v[12:15], v[170:173], v[174:177], v[12:15]
	s_setprio 0
	s_waitcnt vmcnt(8)
	ds_write_b128 v165, v[80:83] offset:40960
	s_waitcnt vmcnt(7)
	ds_write_b128 v165, v[84:87] offset:49152
	s_waitcnt vmcnt(6)
	ds_write_b128 v165, v[88:91] offset:57344
	s_waitcnt vmcnt(5)
	ds_write_b128 v168, v[92:95] offset:24576
	s_waitcnt vmcnt(4)
	ds_write_b128 v168, v[96:99] offset:32768
	v_permlane32_swap_b32_e32 v112, v114
	v_permlane32_swap_b32_e32 v113, v115
	v_permlane32_swap_b32_e32 v116, v118
	v_permlane32_swap_b32_e32 v117, v119
	v_permlane32_swap_b32_e32 v120, v122
	v_permlane32_swap_b32_e32 v121, v123
	v_permlane32_swap_b32_e32 v124, v126
	v_permlane32_swap_b32_e32 v125, v127
	v_cvt_pk_bf16_f32 v80, v112, v116
	v_cvt_pk_bf16_f32 v81, v120, v124
	v_cvt_pk_bf16_f32 v82, v114, v118
	v_cvt_pk_bf16_f32 v83, v122, v126
	v_cvt_pk_bf16_f32 v84, v113, v117
	v_cvt_pk_bf16_f32 v85, v121, v125
	v_cvt_pk_bf16_f32 v86, v115, v119
	v_cvt_pk_bf16_f32 v87, v123, v127
	v_add_u32_e32 v88, s18, v164
	s_lshl_b32 s36, s21, 7
	v_add_u32_e32 v89, s18, v163
	ds_write_b128 v88, v[80:83]
	ds_write_b128 v89, v[84:87]
	v_lshl_add_u64 v[80:81], v[108:109], 0, s[36:37]
	v_add_co_u32_e32 v84, vcc, s70, v80
	s_add_i32 s2, s2, 5
	s_nop 0
	v_addc_co_u32_e32 v85, vcc, 0, v81, vcc
	v_add_co_u32_e32 v88, vcc, s83, v80
	s_and_b32 s21, s2, 7
	s_nop 0
	v_addc_co_u32_e32 v89, vcc, 0, v81, vcc
	v_add_co_u32_e32 v92, vcc, s3, v80
	s_lshl_b32 s36, s21, 19
	s_nop 0
	v_addc_co_u32_e32 v93, vcc, 0, v81, vcc
	v_add_co_u32_e32 v96, vcc, s53, v80
	s_nop 0
	v_addc_co_u32_e32 v97, vcc, 0, v81, vcc
	global_load_dwordx4 v[80:83], v[80:81], off
	s_nop 0
	global_load_dwordx4 v[84:87], v[84:85], off
	s_nop 0
	global_load_dwordx4 v[88:91], v[88:89], off
	s_nop 0
	global_load_dwordx4 v[92:95], v[92:93], off
	s_nop 0
	global_load_dwordx4 v[96:99], v[96:97], off
	v_lshl_add_u64 v[124:125], v[110:111], 0, s[36:37]
	v_add_co_u32_e32 v126, vcc, 0x2000, v124
	s_nop 1
	v_addc_co_u32_e32 v127, vcc, 0, v125, vcc
	v_add_co_u32_e32 v120, vcc, 0x4000, v124
	s_nop 1
	v_addc_co_u32_e32 v121, vcc, 0, v125, vcc
	v_add_co_u32_e32 v122, vcc, 0x6000, v124
	s_nop 1
	v_addc_co_u32_e32 v123, vcc, 0, v125, vcc
	s_waitcnt lgkmcnt(0)
	s_nop 0
	s_barrier
	s_nop 1
	v_add_u32_e32 v144, v169, v162
	s_nop 1
	s_nop 1
	global_load_dwordx4 v[112:115], v[124:125], off
	global_load_dwordx4 v[116:119], v[126:127], off
	global_load_dwordx4 v[124:127], v[122:123], off
	global_load_dwordx4 v[120:123], v[120:121], off
	ds_read_b128 v[146:149], v144
	ds_read_b128 v[150:153], v144 offset:2048
	ds_read_b128 v[154:157], v144 offset:4096
	ds_read_b128 v[170:173], v144 offset:6144
	ds_read_b128 v[174:177], v105 offset:40960
	ds_read_b128 v[178:181], v105 offset:43008
	s_setprio 1
	s_waitcnt lgkmcnt(1)
	v_mfma_f32_16x16x32_bf16 v[76:79], v[146:149], v[174:177], v[76:79]
	v_mfma_f32_16x16x32_bf16 v[72:75], v[150:153], v[174:177], v[72:75]
	v_mfma_f32_16x16x32_bf16 v[68:71], v[154:157], v[174:177], v[68:71]
	v_mfma_f32_16x16x32_bf16 v[64:67], v[170:173], v[174:177], v[64:67]
	s_setprio 0
	ds_read_b128 v[174:177], v105 offset:45056
	s_setprio 1
	s_waitcnt lgkmcnt(1)
	v_mfma_f32_16x16x32_bf16 v[48:51], v[146:149], v[178:181], v[48:51]
	v_mfma_f32_16x16x32_bf16 v[52:55], v[150:153], v[178:181], v[52:55]
	v_mfma_f32_16x16x32_bf16 v[56:59], v[154:157], v[178:181], v[56:59]
	v_mfma_f32_16x16x32_bf16 v[60:63], v[170:173], v[178:181], v[60:63]
	s_setprio 0
	ds_read_b128 v[178:181], v105 offset:47104
	s_setprio 1
	s_waitcnt lgkmcnt(1)
	v_mfma_f32_16x16x32_bf16 v[32:35], v[146:149], v[174:177], v[32:35]
	v_mfma_f32_16x16x32_bf16 v[36:39], v[150:153], v[174:177], v[36:39]
	v_mfma_f32_16x16x32_bf16 v[40:43], v[154:157], v[174:177], v[40:43]
	v_mfma_f32_16x16x32_bf16 v[44:47], v[170:173], v[174:177], v[44:47]
	s_setprio 0
	ds_read_b128 v[174:177], v105 offset:49152
	s_setprio 1
	s_waitcnt lgkmcnt(1)
	v_mfma_f32_16x16x32_bf16 v[16:19], v[146:149], v[178:181], v[16:19]
	v_mfma_f32_16x16x32_bf16 v[20:23], v[150:153], v[178:181], v[20:23]
	v_mfma_f32_16x16x32_bf16 v[24:27], v[154:157], v[178:181], v[24:27]
	v_mfma_f32_16x16x32_bf16 v[28:31], v[170:173], v[178:181], v[28:31]
	s_setprio 0
	s_setprio 1
	s_waitcnt lgkmcnt(0)
	v_mfma_f32_16x16x32_bf16 v[0:3], v[146:149], v[174:177], v[0:3]
	v_mfma_f32_16x16x32_bf16 v[4:7], v[150:153], v[174:177], v[4:7]
	v_mfma_f32_16x16x32_bf16 v[8:11], v[154:157], v[174:177], v[8:11]
	v_mfma_f32_16x16x32_bf16 v[12:15], v[170:173], v[174:177], v[12:15]
	s_setprio 0
	v_add_u32_e32 v105, v169, v161
	ds_read_b128 v[146:149], v105
	ds_read_b128 v[150:153], v105 offset:2048
	ds_read_b128 v[154:157], v105 offset:4096
	ds_read_b128 v[170:173], v105 offset:6144
	ds_read_b128 v[174:177], v107 offset:40960
	ds_read_b128 v[178:181], v107 offset:43008
	s_setprio 1
	s_waitcnt lgkmcnt(1)
	v_mfma_f32_16x16x32_bf16 v[76:79], v[146:149], v[174:177], v[76:79]
	v_mfma_f32_16x16x32_bf16 v[72:75], v[150:153], v[174:177], v[72:75]
	v_mfma_f32_16x16x32_bf16 v[68:71], v[154:157], v[174:177], v[68:71]
	v_mfma_f32_16x16x32_bf16 v[64:67], v[170:173], v[174:177], v[64:67]
	s_setprio 0
	ds_read_b128 v[174:177], v107 offset:45056
	s_setprio 1
	s_waitcnt lgkmcnt(1)
	v_mfma_f32_16x16x32_bf16 v[48:51], v[146:149], v[178:181], v[48:51]
	v_mfma_f32_16x16x32_bf16 v[52:55], v[150:153], v[178:181], v[52:55]
	v_mfma_f32_16x16x32_bf16 v[56:59], v[154:157], v[178:181], v[56:59]
	v_mfma_f32_16x16x32_bf16 v[60:63], v[170:173], v[178:181], v[60:63]
	s_setprio 0
	ds_read_b128 v[178:181], v107 offset:47104
	s_setprio 1
	s_waitcnt lgkmcnt(1)
	v_mfma_f32_16x16x32_bf16 v[32:35], v[146:149], v[174:177], v[32:35]
	v_mfma_f32_16x16x32_bf16 v[36:39], v[150:153], v[174:177], v[36:39]
	v_mfma_f32_16x16x32_bf16 v[40:43], v[154:157], v[174:177], v[40:43]
	v_mfma_f32_16x16x32_bf16 v[44:47], v[170:173], v[174:177], v[44:47]
	s_setprio 0
	ds_read_b128 v[174:177], v107 offset:49152
	s_setprio 1
	s_waitcnt lgkmcnt(1)
	v_mfma_f32_16x16x32_bf16 v[16:19], v[146:149], v[178:181], v[16:19]
	v_mfma_f32_16x16x32_bf16 v[20:23], v[150:153], v[178:181], v[20:23]
	v_mfma_f32_16x16x32_bf16 v[24:27], v[154:157], v[178:181], v[24:27]
	v_mfma_f32_16x16x32_bf16 v[28:31], v[170:173], v[178:181], v[28:31]
	s_setprio 0
	s_setprio 1
	s_waitcnt lgkmcnt(0)
	v_mfma_f32_16x16x32_bf16 v[0:3], v[146:149], v[174:177], v[0:3]
	v_mfma_f32_16x16x32_bf16 v[4:7], v[150:153], v[174:177], v[4:7]
	v_mfma_f32_16x16x32_bf16 v[8:11], v[154:157], v[174:177], v[8:11]
	v_mfma_f32_16x16x32_bf16 v[12:15], v[170:173], v[174:177], v[12:15]
	s_setprio 0
	s_lshl_b32 s36, s21, 7
	s_waitcnt vmcnt(8)
	ds_write_b128 v165, v[80:83]
	s_waitcnt vmcnt(7)
	ds_write_b128 v165, v[84:87] offset:8192
	s_waitcnt vmcnt(6)
	ds_write_b128 v165, v[88:91] offset:16384
	s_waitcnt vmcnt(5)
	ds_write_b128 v165, v[92:95] offset:24576
	s_waitcnt vmcnt(4)
	ds_write_b128 v165, v[96:99] offset:32768
	v_permlane32_swap_b32_e32 v128, v130
	v_permlane32_swap_b32_e32 v129, v131
	v_permlane32_swap_b32_e32 v132, v134
	v_permlane32_swap_b32_e32 v133, v135
	v_permlane32_swap_b32_e32 v136, v138
	v_permlane32_swap_b32_e32 v137, v139
	v_permlane32_swap_b32_e32 v140, v142
	v_permlane32_swap_b32_e32 v141, v143
	v_cvt_pk_bf16_f32 v80, v128, v132
	v_cvt_pk_bf16_f32 v81, v136, v140
	v_cvt_pk_bf16_f32 v82, v130, v134
	v_cvt_pk_bf16_f32 v83, v138, v142
	v_cvt_pk_bf16_f32 v84, v129, v133
	v_cvt_pk_bf16_f32 v85, v137, v141
	v_cvt_pk_bf16_f32 v86, v131, v135
	v_cvt_pk_bf16_f32 v87, v139, v143
	v_lshl_add_u64 v[96:97], v[108:109], 0, s[36:37]
	ds_write_b128 v101, v[80:83]
	ds_write_b128 v103, v[84:87]
	v_add_co_u32_e32 v84, vcc, s70, v96
	global_load_dwordx4 v[80:83], v[96:97], off
	s_nop 0
	v_addc_co_u32_e32 v85, vcc, 0, v97, vcc
	v_add_co_u32_e32 v88, vcc, s83, v96
	global_load_dwordx4 v[84:87], v[84:85], off
	s_nop 0
	v_addc_co_u32_e32 v89, vcc, 0, v97, vcc
	v_add_co_u32_e32 v92, vcc, s3, v96
	global_load_dwordx4 v[88:91], v[88:89], off
	s_nop 0
	v_addc_co_u32_e32 v93, vcc, 0, v97, vcc
	global_load_dwordx4 v[92:95], v[92:93], off
	v_add_co_u32_e32 v96, vcc, s53, v96
	s_add_i32 s15, s15, 2
	s_nop 0
	v_addc_co_u32_e32 v97, vcc, 0, v97, vcc
	global_load_dwordx4 v[96:99], v[96:97], off
	s_cmp_gt_u32 s15, 5
	s_waitcnt lgkmcnt(0)
	s_barrier
	s_cbranch_scc0 .LBB0_1053
	s_waitcnt vmcnt(4)
	v_mov_b32_e32 v80, v145
	s_mov_b64 s[14:15], s[8:9]
	s_mov_b64 s[22:23], s[6:7]
	v_add3_u32 v144, s20, v160, v80
	s_lshl_b64 s[12:13], s[12:13], 1
	v_lshl_add_u64 v[82:83], v[144:145], 2, s[14:15]
	global_load_dword v82, v[82:83], off
	s_add_u32 s2, s22, s12
	s_addc_u32 s13, s23, s13
	s_add_u32 s12, s2, s19
	s_addc_u32 s13, s13, 0
	v_mov_b32_e32 v105, v145
	v_lshl_add_u64 v[80:81], s[12:13], 0, v[104:105]
	v_mov_b32_e32 v107, v145
	s_waitcnt vmcnt(0)
	v_pk_mul_f32 v[70:71], v[70:71], v[82:83] op_sel_hi:[1,0]
	v_pk_mul_f32 v[68:69], v[68:69], v[82:83] op_sel_hi:[1,0]
	v_pk_mul_f32 v[64:65], v[64:65], v[82:83] op_sel_hi:[1,0]
	v_pk_mul_f32 v[78:79], v[78:79], v[82:83] op_sel_hi:[1,0]
	v_pk_mul_f32 v[76:77], v[76:77], v[82:83] op_sel_hi:[1,0]
	v_pk_mul_f32 v[74:75], v[74:75], v[82:83] op_sel_hi:[1,0]
	v_pk_mul_f32 v[72:73], v[72:73], v[82:83] op_sel_hi:[1,0]
	v_cvt_pk_bf16_f32 v68, v68, v69
	v_cvt_pk_bf16_f32 v69, v70, v71
	v_pk_mul_f32 v[66:67], v[66:67], v[82:83] op_sel_hi:[1,0]
	v_cvt_pk_bf16_f32 v70, v64, v65
	v_lshlrev_b64 v[64:65], 12, v[144:145]
	v_cvt_pk_bf16_f32 v76, v76, v77
	v_cvt_pk_bf16_f32 v77, v78, v79
	v_cvt_pk_bf16_f32 v78, v72, v73
	v_cvt_pk_bf16_f32 v79, v74, v75
	v_cvt_pk_bf16_f32 v71, v66, v67
	v_lshl_add_u64 v[64:65], v[80:81], 0, v[64:65]
	v_permlane16_swap_b32_e32 v76, v78
	v_permlane16_swap_b32_e32 v77, v79
	v_lshl_add_u64 v[64:65], v[64:65], 0, v[106:107]
	v_permlane16_swap_b32_e32 v68, v70
	v_permlane16_swap_b32_e32 v69, v71
	global_store_dwordx4 v[64:65], v[76:79], off
	global_store_dwordx4 v[64:65], v[68:71], off offset:64
	v_add_u32_e32 v64, 16, v144
	v_mov_b32_e32 v65, v145
	v_lshl_add_u64 v[66:67], v[64:65], 2, s[14:15]
	global_load_dword v66, v[66:67], off
	s_waitcnt vmcnt(0)
	v_pk_mul_f32 v[50:51], v[50:51], v[66:67] op_sel_hi:[1,0]
	v_pk_mul_f32 v[48:49], v[48:49], v[66:67] op_sel_hi:[1,0]
	v_pk_mul_f32 v[54:55], v[54:55], v[66:67] op_sel_hi:[1,0]
	v_cvt_pk_bf16_f32 v48, v48, v49
	v_cvt_pk_bf16_f32 v49, v50, v51
	v_pk_mul_f32 v[50:51], v[52:53], v[66:67] op_sel_hi:[1,0]
	v_pk_mul_f32 v[52:53], v[56:57], v[66:67] op_sel_hi:[1,0]
	v_cvt_pk_bf16_f32 v50, v50, v51
	v_cvt_pk_bf16_f32 v51, v54, v55
	v_pk_mul_f32 v[54:55], v[58:59], v[66:67] op_sel_hi:[1,0]
	v_cvt_pk_bf16_f32 v52, v52, v53
	v_cvt_pk_bf16_f32 v53, v54, v55
	v_pk_mul_f32 v[56:57], v[62:63], v[66:67] op_sel_hi:[1,0]
	v_pk_mul_f32 v[54:55], v[60:61], v[66:67] op_sel_hi:[1,0]
	v_permlane16_swap_b32_e32 v48, v50
	v_cvt_pk_bf16_f32 v54, v54, v55
	v_cvt_pk_bf16_f32 v55, v56, v57
	v_lshlrev_b64 v[56:57], 12, v[64:65]
	v_lshl_add_u64 v[56:57], v[80:81], 0, v[56:57]
	v_permlane16_swap_b32_e32 v49, v51
	v_lshl_add_u64 v[56:57], v[56:57], 0, v[106:107]
	global_store_dwordx4 v[56:57], v[48:51], off
	v_permlane16_swap_b32_e32 v52, v54
	v_permlane16_swap_b32_e32 v53, v55
	v_add_u32_e32 v48, 32, v144
	v_mov_b32_e32 v49, v145
	global_store_dwordx4 v[56:57], v[52:55], off offset:64
	v_lshl_add_u64 v[50:51], v[48:49], 2, s[14:15]
	global_load_dword v50, v[50:51], off
	s_waitcnt vmcnt(0)
	v_pk_mul_f32 v[34:35], v[34:35], v[50:51] op_sel_hi:[1,0]
	v_pk_mul_f32 v[32:33], v[32:33], v[50:51] op_sel_hi:[1,0]
	v_pk_mul_f32 v[38:39], v[38:39], v[50:51] op_sel_hi:[1,0]
	v_cvt_pk_bf16_f32 v32, v32, v33
	v_cvt_pk_bf16_f32 v33, v34, v35
	v_pk_mul_f32 v[34:35], v[36:37], v[50:51] op_sel_hi:[1,0]
	v_pk_mul_f32 v[36:37], v[40:41], v[50:51] op_sel_hi:[1,0]
	v_cvt_pk_bf16_f32 v34, v34, v35
	v_cvt_pk_bf16_f32 v35, v38, v39
	v_pk_mul_f32 v[38:39], v[42:43], v[50:51] op_sel_hi:[1,0]
	v_cvt_pk_bf16_f32 v36, v36, v37
	v_cvt_pk_bf16_f32 v37, v38, v39
	v_pk_mul_f32 v[40:41], v[46:47], v[50:51] op_sel_hi:[1,0]
	v_pk_mul_f32 v[38:39], v[44:45], v[50:51] op_sel_hi:[1,0]
	v_permlane16_swap_b32_e32 v32, v34
	v_cvt_pk_bf16_f32 v38, v38, v39
	v_cvt_pk_bf16_f32 v39, v40, v41
	v_lshlrev_b64 v[40:41], 12, v[48:49]
	v_lshl_add_u64 v[40:41], v[80:81], 0, v[40:41]
	v_permlane16_swap_b32_e32 v33, v35
	v_lshl_add_u64 v[40:41], v[40:41], 0, v[106:107]
	global_store_dwordx4 v[40:41], v[32:35], off
	v_permlane16_swap_b32_e32 v36, v38
	v_permlane16_swap_b32_e32 v37, v39
	v_add_u32_e32 v32, 48, v144
	v_mov_b32_e32 v33, v145
	global_store_dwordx4 v[40:41], v[36:39], off offset:64
	v_lshl_add_u64 v[34:35], v[32:33], 2, s[14:15]
	global_load_dword v34, v[34:35], off
	v_add_u32_e32 v144, 64, v144
	s_waitcnt vmcnt(0)
	v_pk_mul_f32 v[18:19], v[18:19], v[34:35] op_sel_hi:[1,0]
	v_pk_mul_f32 v[16:17], v[16:17], v[34:35] op_sel_hi:[1,0]
	v_pk_mul_f32 v[22:23], v[22:23], v[34:35] op_sel_hi:[1,0]
	v_cvt_pk_bf16_f32 v16, v16, v17
	v_cvt_pk_bf16_f32 v17, v18, v19
	v_pk_mul_f32 v[18:19], v[20:21], v[34:35] op_sel_hi:[1,0]
	v_pk_mul_f32 v[20:21], v[24:25], v[34:35] op_sel_hi:[1,0]
	v_cvt_pk_bf16_f32 v18, v18, v19
	v_cvt_pk_bf16_f32 v19, v22, v23
	v_pk_mul_f32 v[22:23], v[26:27], v[34:35] op_sel_hi:[1,0]
	v_cvt_pk_bf16_f32 v20, v20, v21
	v_cvt_pk_bf16_f32 v21, v22, v23
	v_pk_mul_f32 v[24:25], v[30:31], v[34:35] op_sel_hi:[1,0]
	v_pk_mul_f32 v[22:23], v[28:29], v[34:35] op_sel_hi:[1,0]
	v_permlane16_swap_b32_e32 v16, v18
	v_cvt_pk_bf16_f32 v22, v22, v23
	v_cvt_pk_bf16_f32 v23, v24, v25
	v_lshlrev_b64 v[24:25], 12, v[32:33]
	v_lshl_add_u64 v[24:25], v[80:81], 0, v[24:25]
	v_permlane16_swap_b32_e32 v17, v19
	v_lshl_add_u64 v[24:25], v[24:25], 0, v[106:107]
	v_permlane16_swap_b32_e32 v20, v22
	v_permlane16_swap_b32_e32 v21, v23
	global_store_dwordx4 v[24:25], v[16:19], off
	global_store_dwordx4 v[24:25], v[20:23], off offset:64
	s_nop 0
	v_lshl_add_u64 v[16:17], v[144:145], 2, s[14:15]
	global_load_dword v16, v[16:17], off
	s_waitcnt vmcnt(0)
	v_pk_mul_f32 v[2:3], v[2:3], v[16:17] op_sel_hi:[1,0]
	v_pk_mul_f32 v[0:1], v[0:1], v[16:17] op_sel_hi:[1,0]
	v_pk_mul_f32 v[6:7], v[6:7], v[16:17] op_sel_hi:[1,0]
	v_cvt_pk_bf16_f32 v0, v0, v1
	v_cvt_pk_bf16_f32 v1, v2, v3
	v_pk_mul_f32 v[2:3], v[4:5], v[16:17] op_sel_hi:[1,0]
	v_pk_mul_f32 v[4:5], v[8:9], v[16:17] op_sel_hi:[1,0]
	v_cvt_pk_bf16_f32 v2, v2, v3
	v_cvt_pk_bf16_f32 v3, v6, v7
	v_pk_mul_f32 v[6:7], v[10:11], v[16:17] op_sel_hi:[1,0]
	v_cvt_pk_bf16_f32 v4, v4, v5
	v_cvt_pk_bf16_f32 v5, v6, v7
	v_pk_mul_f32 v[8:9], v[14:15], v[16:17] op_sel_hi:[1,0]
	v_pk_mul_f32 v[6:7], v[12:13], v[16:17] op_sel_hi:[1,0]
	v_permlane16_swap_b32_e32 v0, v2
	v_cvt_pk_bf16_f32 v6, v6, v7
	v_cvt_pk_bf16_f32 v7, v8, v9
	v_lshlrev_b64 v[8:9], 12, v[144:145]
	v_lshl_add_u64 v[8:9], v[80:81], 0, v[8:9]
	v_permlane16_swap_b32_e32 v1, v3
	v_lshl_add_u64 v[8:9], v[8:9], 0, v[106:107]
	v_permlane16_swap_b32_e32 v4, v6
	v_permlane16_swap_b32_e32 v5, v7
	global_store_dwordx4 v[8:9], v[0:3], off
	global_store_dwordx4 v[8:9], v[4:7], off offset:64
	s_branch .LBB0_1050
